# rowpass: software prefetch of next row MIX + x first half
# speedup vs baseline: 1.0049x; 1.0049x over previous
; DI void pv_all_sm(f32x16* o, int vb, bf16x8 pa0, bf16x8 pa1, bf16x8 pa2, bf16x8 pa3, f32x16& p0, f32x16& p1, float& m_ref, f32x16& negm, float& alpha) {
;     ...
;     pv_one<3>(o[3], vb, pa0, pa1, pa2, pa3);
; #pragma unroll
;     for (int r = 0; r < 16; ++r) p0[r] = __builtin_amdgcn_exp2f(p0[r]);
.LBB4_706:
	ds_read_b64_tr_b16 v[214:215], v186 offset:0x600
	ds_read_b64_tr_b16 v[216:217], v186 offset:0xe00
	ds_read_b64_tr_b16 v[218:219], v186 offset:0x1600
	ds_read_b64_tr_b16 v[220:221], v186 offset:0x1e00
	ds_read_b64_tr_b16 v[222:223], v186 offset:0x2600
	ds_read_b64_tr_b16 v[224:225], v186 offset:0x2e00
	ds_read_b64_tr_b16 v[226:227], v186 offset:0x3600
	ds_read_b64_tr_b16 v[228:229], v186 offset:0x3e00
	s_waitcnt lgkmcnt(0)
	s_nop 0
	v_mfma_f32_32x32x16_bf16 v[0:15], v[214:217], v[96:99], v[0:15]
	s_lshl_b32 s2, s64, 14
	s_add_i32 s2, s2, 0
	s_lshl_b32 s3, s64, 13
	v_add_u32_e32 v96, s2, v200
	s_sub_i32 s78, s2, s3
	s_waitcnt vmcnt(0)
	v_add_u32_e32 v97, s2, v201
	v_mfma_f32_32x32x16_bf16 v[0:15], v[218:221], v[108:111], v[0:15]
	s_waitcnt vmcnt(2)
	ds_write_b128 v96, v[176:179]
	v_add_u32_e32 v96, s78, v202
	s_waitcnt vmcnt(1)
	ds_write_b128 v97, v[172:175]
	s_waitcnt vmcnt(0)
	ds_write_b128 v96, v[168:171] offset:49152
	v_cndmask_b32_e64 v96, 0, 1, s[34:35]
	v_cmp_ne_u32_e64 s[2:3], 1, v96
	s_andn2_b64 vcc, exec, s[34:35]
	v_mfma_f32_32x32x16_bf16 v[0:15], v[222:225], v[100:103], v[0:15]
	v_mfma_f32_32x32x16_bf16 v[0:15], v[226:229], v[104:107], v[0:15]
	s_cbranch_vccnz .LBB4_711
	v_mul_f32_e32 v97, 0x44000000, v160
	v_mul_f32_e32 v98, 0x44000000, v164
	v_med3_f32 v97, v97, s62, v211
	v_med3_f32 v98, v98, s62, v211
	v_mov_b32_e32 v99, 0
	v_cvt_pk_fp8_f32 v99, v97, v98
	v_mul_f32_e32 v97, 0x44000000, v161
	v_mul_f32_e32 v98, 0x44000000, v165
	v_med3_f32 v97, v97, s62, v211
	v_med3_f32 v98, v98, s62, v211
	v_mov_b32_e32 v100, 0
	v_cvt_pk_fp8_f32 v100, v97, v98
	v_mul_f32_e32 v97, 0x44000000, v162
	v_mul_f32_e32 v98, 0x44000000, v166
	v_med3_f32 v97, v97, s62, v211
	v_med3_f32 v98, v98, s62, v211
	v_mov_b32_e32 v101, 0
	s_bitcmp1_b32 s58, 0
	v_cvt_pk_fp8_f32 v101, v97, v98
	v_mul_f32_e32 v97, 0x44000000, v163
	v_mul_f32_e32 v98, 0x44000000, v167
	s_cselect_b32 s8, 0x1100, 0
	v_med3_f32 v97, v97, s62, v211
	v_med3_f32 v98, v98, s62, v211
	v_mov_b32_e32 v102, 0
	v_cmp_eq_u32_e32 vcc, 0, v181
	v_add_u32_e32 v96, s8, v191
	v_cvt_pk_fp8_f32 v102, v97, v98
	s_and_b64 vcc, exec, vcc
	s_and_b32 s34, s58, 31
	ds_write_b16 v96, v99
	ds_write_b16 v96, v100 offset:68
	ds_write_b16 v96, v101 offset:136
	ds_write_b16 v96, v102 offset:204
	s_cbranch_vccnz .LBB4_735
	s_lshl_b32 s8, s34, 7
	s_lshl_b32 s9, s58, 6
	s_and_b32 s8, s8, 0xf00
	s_and_b32 s9, s9, 64
	s_or_b32 s26, s8, s9
	s_cbranch_execnz .LBB4_710

; DI void finishSM(f32x16& p0, f32x16& p1, float alpha, float& l_reg, bf16x8& pa0, bf16x8& pa1, bf16x8& pa2, bf16x8& pa3) {
; #pragma unroll
;     for (int r = 0; r < 16; ++r) p1[r] = __builtin_amdgcn_exp2f(p1[r]);
;     float ps = 0;
; #pragma unroll
;     for (int r = 0; r < 16; ++r) ps += p0[r];
; #pragma unroll
;     for (int r = 0; r < 16; ++r) ps += p1[r];
;     { auto rr = __builtin_amdgcn_permlane32_swap(__float_as_uint(ps), __float_as_uint(ps), false, false); ps = __uint_as_float(rr[0]) + __uint_as_float(rr[1]); }
;     l_reg = l_reg * alpha + ps;
;     ...
;     AT_PK4(p0, 0, pa0); AT_PK4(p0, 8, pa1); AT_PK4(p1, 0, pa2); AT_PK4(p1, 8, pa3);
;     ...
; }
; DI void qkt(f32x16& p0, f32x16& p1, const char* Ks, const bf16x8* qr, const f32x16& negm, int r32, int hi) {
; #pragma unroll
;     for (int d0 = 0; d0 < 4; ++d0) { const int cb = (d0 * 16 + hi * 8) * 2;
;         const bf16x8 b0 = *reinterpret_cast<const bf16x8*>(Ks + AT_KSWZ(r32, cb));
;         const bf16x8 b1 = *reinterpret_cast<const bf16x8*>(Ks + AT_KSWZ(32 + r32, cb));
;         p0 = __builtin_amdgcn_mfma_f32_32x32x16_bf16(b0, qr[d0], d0 == 0 ? negm : p0, 0, 0, 0);
;         p1 = __builtin_amdgcn_mfma_f32_32x32x16_bf16(b1, qr[d0], d0 == 0 ? negm : p1, 0, 0, 0); }
; DI void attn_pass(const Frame& F, CvRide& cv, const bf16_t* __restrict__ Qb, const bf16_t* __restrict__ Kh, const bf16_t* __restrict__ Vh, char* lds, f32x16 (&o)[4], float& l_out, const int wave_s) {
;     ...
;     const unsigned cv_ldo = (unsigned)(((tid >> 4) * 2 * 2048 + (tid & 15) * 4) * 4), cv_sto = (unsigned)((tid >> 3) * 2048 + 8 * (tid & 7));
;     const int cv_lw = OFF_CV + (4 * (tid & 15)) * 68 + 2 * (tid >> 4), cv_lr = OFF_CV + (tid >> 3) * 68 + 8 * (tid & 7);
;     f32x4 cvA = f32x4{}, cvB = f32x4{}; unsigned cvr0 = 0, cvr1 = 0;
.LBB4_723:
	v_exp_f32_e32 v186, v128
	v_exp_f32_e32 v230, v129
	v_exp_f32_e32 v231, v130
	v_exp_f32_e32 v232, v131
	v_exp_f32_e32 v233, v132
	v_exp_f32_e32 v234, v133
	v_exp_f32_e32 v235, v134
	v_exp_f32_e32 v236, v135
	v_exp_f32_e32 v237, v136
	v_exp_f32_e32 v238, v137
	v_exp_f32_e32 v239, v138
	v_exp_f32_e32 v240, v139
	v_exp_f32_e32 v241, v140
	v_exp_f32_e32 v242, v141
	v_exp_f32_e32 v243, v142
	v_exp_f32_e32 v244, v143
	v_add_u32_e32 v100, s78, v204
	ds_read_b128 v[96:99], v100 offset:49152
	ds_read_b128 v[168:171], v100 offset:53248
	v_add_u32_e32 v101, s78, v205
	v_add_u32_e32 v102, s78, v206
	v_add_u32_e32 v103, s78, v207
	ds_read_b128 v[172:175], v101 offset:49152
	ds_read_b128 v[176:179], v101 offset:53248
	ds_read_b128 v[214:217], v102 offset:49152
	ds_read_b128 v[218:221], v102 offset:53248
	ds_read_b128 v[222:225], v103 offset:49152
	ds_read_b128 v[226:229], v103 offset:53248
	v_exp_f32_e32 v112, v112
	v_exp_f32_e32 v113, v113
	v_exp_f32_e32 v114, v114
	s_waitcnt lgkmcnt(7)
	v_mfma_f32_32x32x16_bf16 v[128:143], v[96:99], v[156:159], v[64:79]
	v_exp_f32_e32 v115, v115
	v_exp_f32_e32 v116, v116
	v_exp_f32_e32 v117, v117
	v_exp_f32_e32 v118, v118
	v_exp_f32_e32 v119, v119
	s_waitcnt lgkmcnt(6)
	v_mfma_f32_32x32x16_bf16 v[96:111], v[168:171], v[156:159], v[64:79]
	v_exp_f32_e32 v168, v120
	v_add_f32_e32 v120, 0, v186
	v_add_f32_e32 v120, v230, v120
	v_add_f32_e32 v120, v231, v120
	v_add_f32_e32 v120, v232, v120
	v_add_f32_e32 v120, v233, v120
	v_add_f32_e32 v120, v234, v120
	v_add_f32_e32 v120, v235, v120
	v_add_f32_e32 v120, v236, v120
	v_add_f32_e32 v120, v237, v120
	v_add_f32_e32 v120, v238, v120
	s_waitcnt lgkmcnt(5)
	v_mfma_f32_32x32x16_bf16 v[128:143], v[172:175], v[152:155], v[128:143]
	v_add_f32_e32 v120, v239, v120
	v_add_f32_e32 v120, v240, v120
	v_add_f32_e32 v120, v241, v120
	v_add_f32_e32 v120, v242, v120
	v_add_f32_e32 v120, v243, v120
	v_add_f32_e32 v120, v244, v120
	v_add_f32_e32 v120, v112, v120
	s_waitcnt lgkmcnt(4)
	v_mfma_f32_32x32x16_bf16 v[96:111], v[176:179], v[152:155], v[96:111]
	v_add_f32_e32 v120, v113, v120
	v_add_f32_e32 v120, v114, v120
	v_add_f32_e32 v120, v115, v120
	v_add_f32_e32 v120, v116, v120
	v_exp_f32_e32 v169, v121
	v_add_f32_e32 v120, v117, v120
	v_exp_f32_e32 v170, v122
	s_waitcnt lgkmcnt(3)
	v_mfma_f32_32x32x16_bf16 v[128:143], v[214:217], v[148:151], v[128:143]
	v_add_f32_e32 v120, v118, v120
	v_exp_f32_e32 v171, v123
	v_add_f32_e32 v120, v119, v120
	v_exp_f32_e32 v172, v124
	v_add_f32_e32 v120, v168, v120
	v_exp_f32_e32 v173, v125
	v_add_f32_e32 v120, v169, v120
	s_waitcnt lgkmcnt(2)
	v_mfma_f32_32x32x16_bf16 v[96:111], v[218:221], v[148:151], v[96:111]
	v_exp_f32_e32 v174, v126
	v_add_f32_e32 v120, v170, v120
	v_exp_f32_e32 v175, v127
	v_add_f32_e32 v120, v171, v120
	v_add_f32_e32 v120, v172, v120
	v_add_f32_e32 v120, v173, v120
	v_add_f32_e32 v120, v174, v120
	s_waitcnt lgkmcnt(1)
	v_mfma_f32_32x32x16_bf16 v[128:143], v[222:225], v[144:147], v[128:143]
	v_add_f32_e32 v213, v175, v120
	v_mov_b32_e32 v214, v213
	v_cvt_pk_bf16_f32 v120, v186, v230
	v_cvt_pk_bf16_f32 v121, v231, v232
	v_cvt_pk_bf16_f32 v122, v233, v234
	v_cvt_pk_bf16_f32 v123, v235, v236
	v_cvt_pk_bf16_f32 v124, v237, v238
	s_waitcnt lgkmcnt(0)
	v_mfma_f32_32x32x16_bf16 v[96:111], v[226:229], v[144:147], v[96:111]
	v_cvt_pk_bf16_f32 v125, v239, v240
	v_cvt_pk_bf16_f32 v126, v241, v242
	v_cvt_pk_bf16_f32 v127, v243, v244
	v_cvt_pk_bf16_f32 v112, v112, v113
	v_cvt_pk_bf16_f32 v113, v114, v115
	v_cvt_pk_bf16_f32 v114, v116, v117
	v_cvt_pk_bf16_f32 v115, v118, v119
	v_cvt_pk_bf16_f32 v116, v168, v169
	v_cvt_pk_bf16_f32 v117, v170, v171
	v_cvt_pk_bf16_f32 v118, v172, v173
	v_cvt_pk_bf16_f32 v119, v174, v175
	v_permlane32_swap_b32_e32 v213, v214
	v_permlane32_swap_b32_e32 v120, v122
	v_permlane32_swap_b32_e32 v121, v123
	v_permlane32_swap_b32_e32 v124, v126
	v_permlane32_swap_b32_e32 v125, v127
	v_permlane32_swap_b32_e32 v112, v114
	v_permlane32_swap_b32_e32 v113, v115
	v_permlane32_swap_b32_e32 v116, v118
	v_permlane32_swap_b32_e32 v117, v119
	s_add_u32 s78, s74, 0x2380c000
	s_addc_u32 s79, s75, 0
	s_add_u32 s74, s74, 0x2380e000
	s_addc_u32 s75, s75, 0
	s_add_u32 s76, s76, 0x21806000
	s_addc_u32 s77, s77, 0
	v_mov_b32_e32 v168, v198
	v_mov_b32_e32 v169, v197
	global_load_dwordx4 v[176:179], v169, s[78:79]
	global_load_dwordx4 v[172:175], v169, s[74:75]
	s_nop 0
	global_load_dwordx4 v[168:171], v168, s[76:77]
	s_and_b64 vcc, exec, s[2:3]
	s_cbranch_vccnz .LBB4_725
	s_mov_b64 s[2:3], s[8:9]
	v_mov_b32_e32 v186, v189
	global_store_dwordx2 v186, v[184:185], s[2:3] nt

; DI void pv_all_sm(f32x16* o, int vb, bf16x8 pa0, bf16x8 pa1, bf16x8 pa2, bf16x8 pa3, f32x16& p0, f32x16& p1, float& m_ref, f32x16& negm, float& alpha) {
;     ...
;     pv_one<3>(o[3], vb, pa0, pa1, pa2, pa3);
; #pragma unroll
;     for (int r = 0; r < 16; ++r) p0[r] = __builtin_amdgcn_exp2f(p0[r]);
.LBB4_779:
	ds_read_b64_tr_b16 v[218:219], v182 offset:0x600
	ds_read_b64_tr_b16 v[220:221], v182 offset:0xe00
	ds_read_b64_tr_b16 v[222:223], v182 offset:0x1600
	ds_read_b64_tr_b16 v[224:225], v182 offset:0x1e00
	ds_read_b64_tr_b16 v[226:227], v182 offset:0x2600
	ds_read_b64_tr_b16 v[228:229], v182 offset:0x2e00
	ds_read_b64_tr_b16 v[230:231], v182 offset:0x3600
	ds_read_b64_tr_b16 v[232:233], v182 offset:0x3e00
	s_waitcnt lgkmcnt(0)
	s_nop 0
	v_mfma_f32_32x32x16_bf16 v[0:15], v[218:221], v[96:99], v[0:15]
	s_lshl_b32 s2, s15, 14
	s_add_i32 s2, s2, 0
	s_lshl_b32 s3, s15, 13
	v_add_u32_e32 v96, s2, v203
	s_sub_i32 s65, s2, s3
	s_waitcnt vmcnt(0)
	v_add_u32_e32 v97, s2, v204
	v_mfma_f32_32x32x16_bf16 v[0:15], v[222:225], v[108:111], v[0:15]
	s_waitcnt vmcnt(2)
	ds_write_b128 v96, v[176:179]
	v_add_u32_e32 v96, s65, v205
	s_waitcnt vmcnt(1)
	ds_write_b128 v97, v[172:175]
	s_waitcnt vmcnt(0)
	ds_write_b128 v96, v[168:171] offset:49152
	v_cndmask_b32_e64 v96, 0, 1, s[22:23]
	v_cmp_ne_u32_e64 s[2:3], 1, v96
	s_andn2_b64 vcc, exec, s[22:23]
	v_mfma_f32_32x32x16_bf16 v[0:15], v[226:229], v[100:103], v[0:15]
	v_mfma_f32_32x32x16_bf16 v[0:15], v[230:233], v[104:107], v[0:15]
	s_cbranch_vccnz .LBB4_784
	v_mul_f32_e32 v97, 0x44000000, v160
	v_mul_f32_e32 v98, 0x44000000, v164
	v_med3_f32 v97, v97, s28, v214
	v_med3_f32 v98, v98, s28, v214
	v_mov_b32_e32 v99, 0
	v_cvt_pk_fp8_f32 v99, v97, v98
	v_mul_f32_e32 v97, 0x44000000, v161
	v_mul_f32_e32 v98, 0x44000000, v165
	v_med3_f32 v97, v97, s28, v214
	v_med3_f32 v98, v98, s28, v214
	v_mov_b32_e32 v100, 0
	v_cvt_pk_fp8_f32 v100, v97, v98
	v_mul_f32_e32 v97, 0x44000000, v162
	v_mul_f32_e32 v98, 0x44000000, v166
	v_med3_f32 v97, v97, s28, v214
	v_med3_f32 v98, v98, s28, v214
	v_mov_b32_e32 v101, 0
	s_bitcmp1_b32 s58, 0
	v_cvt_pk_fp8_f32 v101, v97, v98
	v_mul_f32_e32 v97, 0x44000000, v163
	v_mul_f32_e32 v98, 0x44000000, v167
	s_cselect_b32 s8, 0x1100, 0
	v_med3_f32 v97, v97, s28, v214
	v_med3_f32 v98, v98, s28, v214
	v_mov_b32_e32 v102, 0
	v_cmp_eq_u32_e32 vcc, 0, v181
	v_add_u32_e32 v96, s8, v195
	v_cvt_pk_fp8_f32 v102, v97, v98
	s_and_b64 vcc, exec, vcc
	s_and_b32 s22, s58, 31
	ds_write_b16 v96, v99
	ds_write_b16 v96, v100 offset:68
	ds_write_b16 v96, v101 offset:136
	ds_write_b16 v96, v102 offset:204
	s_cbranch_vccnz .LBB4_808
	s_lshl_b32 s8, s22, 7
	s_lshl_b32 s9, s58, 6
	s_and_b32 s8, s8, 0xf00
	s_and_b32 s9, s9, 64
	s_or_b32 s20, s8, s9
	s_cbranch_execnz .LBB4_783

; DI void finishSM(f32x16& p0, f32x16& p1, float alpha, float& l_reg, bf16x8& pa0, bf16x8& pa1, bf16x8& pa2, bf16x8& pa3) {
; #pragma unroll
;     for (int r = 0; r < 16; ++r) p1[r] = __builtin_amdgcn_exp2f(p1[r]);
;     float ps = 0;
; #pragma unroll
;     for (int r = 0; r < 16; ++r) ps += p0[r];
; #pragma unroll
;     for (int r = 0; r < 16; ++r) ps += p1[r];
;     { auto rr = __builtin_amdgcn_permlane32_swap(__float_as_uint(ps), __float_as_uint(ps), false, false); ps = __uint_as_float(rr[0]) + __uint_as_float(rr[1]); }
;     l_reg = l_reg * alpha + ps;
;     ...
;     AT_PK4(p0, 0, pa0); AT_PK4(p0, 8, pa1); AT_PK4(p1, 0, pa2); AT_PK4(p1, 8, pa3);
;     ...
; }
; DI void qkt(f32x16& p0, f32x16& p1, const char* Ks, const bf16x8* qr, const f32x16& negm, int r32, int hi) {
; #pragma unroll
;     for (int d0 = 0; d0 < 4; ++d0) { const int cb = (d0 * 16 + hi * 8) * 2;
;         const bf16x8 b0 = *reinterpret_cast<const bf16x8*>(Ks + AT_KSWZ(r32, cb));
;         const bf16x8 b1 = *reinterpret_cast<const bf16x8*>(Ks + AT_KSWZ(32 + r32, cb));
;         p0 = __builtin_amdgcn_mfma_f32_32x32x16_bf16(b0, qr[d0], d0 == 0 ? negm : p0, 0, 0, 0);
;         p1 = __builtin_amdgcn_mfma_f32_32x32x16_bf16(b1, qr[d0], d0 == 0 ? negm : p1, 0, 0, 0); }
; DI void attn_pass(const Frame& F, CvRide& cv, const bf16_t* __restrict__ Qb, const bf16_t* __restrict__ Kh, const bf16_t* __restrict__ Vh, char* lds, f32x16 (&o)[4], float& l_out, const int wave_s) {
;     ...
;     const unsigned cv_ldo = (unsigned)(((tid >> 4) * 2 * 2048 + (tid & 15) * 4) * 4), cv_sto = (unsigned)((tid >> 3) * 2048 + 8 * (tid & 7));
;     const int cv_lw = OFF_CV + (4 * (tid & 15)) * 68 + 2 * (tid >> 4), cv_lr = OFF_CV + (tid >> 3) * 68 + 8 * (tid & 7);
;     f32x4 cvA = f32x4{}, cvB = f32x4{}; unsigned cvr0 = 0, cvr1 = 0;
.LBB4_796:
	v_exp_f32_e32 v182, v128
	v_exp_f32_e32 v234, v129
	v_exp_f32_e32 v235, v130
	v_exp_f32_e32 v236, v131
	v_exp_f32_e32 v237, v132
	v_exp_f32_e32 v238, v133
	v_exp_f32_e32 v239, v134
	v_exp_f32_e32 v240, v135
	v_exp_f32_e32 v241, v136
	v_exp_f32_e32 v242, v137
	v_exp_f32_e32 v243, v138
	v_exp_f32_e32 v244, v139
	v_exp_f32_e32 v245, v140
	v_exp_f32_e32 v246, v141
	v_exp_f32_e32 v247, v142
	v_exp_f32_e32 v248, v143
	v_add_u32_e32 v100, s65, v207
	ds_read_b128 v[96:99], v100 offset:49152
	ds_read_b128 v[168:171], v100 offset:53248
	v_add_u32_e32 v101, s65, v208
	v_add_u32_e32 v102, s65, v209
	v_add_u32_e32 v103, s65, v210
	ds_read_b128 v[172:175], v101 offset:49152
	ds_read_b128 v[176:179], v101 offset:53248
	ds_read_b128 v[218:221], v102 offset:49152
	ds_read_b128 v[222:225], v102 offset:53248
	ds_read_b128 v[226:229], v103 offset:49152
	ds_read_b128 v[230:233], v103 offset:53248
	v_exp_f32_e32 v112, v112
	v_exp_f32_e32 v113, v113
	v_exp_f32_e32 v114, v114
	s_waitcnt lgkmcnt(7)
	v_mfma_f32_32x32x16_bf16 v[128:143], v[96:99], v[156:159], v[64:79]
	v_exp_f32_e32 v115, v115
	v_exp_f32_e32 v116, v116
	v_exp_f32_e32 v117, v117
	v_exp_f32_e32 v118, v118
	v_exp_f32_e32 v119, v119
	s_waitcnt lgkmcnt(6)
	v_mfma_f32_32x32x16_bf16 v[96:111], v[168:171], v[156:159], v[64:79]
	v_exp_f32_e32 v168, v120
	v_add_f32_e32 v120, 0, v182
	v_add_f32_e32 v120, v234, v120
	v_add_f32_e32 v120, v235, v120
	v_add_f32_e32 v120, v236, v120
	v_add_f32_e32 v120, v237, v120
	v_add_f32_e32 v120, v238, v120
	v_add_f32_e32 v120, v239, v120
	v_add_f32_e32 v120, v240, v120
	v_add_f32_e32 v120, v241, v120
	v_add_f32_e32 v120, v242, v120
	s_waitcnt lgkmcnt(5)
	v_mfma_f32_32x32x16_bf16 v[128:143], v[172:175], v[152:155], v[128:143]
	v_add_f32_e32 v120, v243, v120
	v_add_f32_e32 v120, v244, v120
	v_add_f32_e32 v120, v245, v120
	v_add_f32_e32 v120, v246, v120
	v_add_f32_e32 v120, v247, v120
	v_add_f32_e32 v120, v248, v120
	v_add_f32_e32 v120, v112, v120
	s_waitcnt lgkmcnt(4)
	v_mfma_f32_32x32x16_bf16 v[96:111], v[176:179], v[152:155], v[96:111]
	v_add_f32_e32 v120, v113, v120
	v_add_f32_e32 v120, v114, v120
	v_add_f32_e32 v120, v115, v120
	v_add_f32_e32 v120, v116, v120
	v_exp_f32_e32 v169, v121
	v_add_f32_e32 v120, v117, v120
	v_exp_f32_e32 v170, v122
	s_waitcnt lgkmcnt(3)
	v_mfma_f32_32x32x16_bf16 v[128:143], v[218:221], v[148:151], v[128:143]
	v_add_f32_e32 v120, v118, v120
	v_exp_f32_e32 v171, v123
	v_add_f32_e32 v120, v119, v120
	v_exp_f32_e32 v172, v124
	v_add_f32_e32 v120, v168, v120
	v_exp_f32_e32 v173, v125
	v_add_f32_e32 v120, v169, v120
	s_waitcnt lgkmcnt(2)
	v_mfma_f32_32x32x16_bf16 v[96:111], v[222:225], v[148:151], v[96:111]
	v_exp_f32_e32 v174, v126
	v_add_f32_e32 v120, v170, v120
	v_exp_f32_e32 v175, v127
	v_add_f32_e32 v120, v171, v120
	v_add_f32_e32 v120, v172, v120
	v_add_f32_e32 v120, v173, v120
	v_add_f32_e32 v120, v174, v120
	s_waitcnt lgkmcnt(1)
	v_mfma_f32_32x32x16_bf16 v[128:143], v[226:229], v[144:147], v[128:143]
	v_add_f32_e32 v217, v175, v120
	v_mov_b32_e32 v218, v217
	v_cvt_pk_bf16_f32 v120, v182, v234
	v_cvt_pk_bf16_f32 v121, v235, v236
	v_cvt_pk_bf16_f32 v122, v237, v238
	v_cvt_pk_bf16_f32 v123, v239, v240
	v_cvt_pk_bf16_f32 v124, v241, v242
	s_waitcnt lgkmcnt(0)
	v_mfma_f32_32x32x16_bf16 v[96:111], v[230:233], v[144:147], v[96:111]
	v_cvt_pk_bf16_f32 v125, v243, v244
	v_cvt_pk_bf16_f32 v126, v245, v246
	v_cvt_pk_bf16_f32 v127, v247, v248
	v_cvt_pk_bf16_f32 v112, v112, v113
	v_cvt_pk_bf16_f32 v113, v114, v115
	v_cvt_pk_bf16_f32 v114, v116, v117
	v_cvt_pk_bf16_f32 v115, v118, v119
	v_cvt_pk_bf16_f32 v116, v168, v169
	v_cvt_pk_bf16_f32 v117, v170, v171
	v_cvt_pk_bf16_f32 v118, v172, v173
	v_cvt_pk_bf16_f32 v119, v174, v175
	v_permlane32_swap_b32_e32 v217, v218
	v_permlane32_swap_b32_e32 v120, v122
	v_permlane32_swap_b32_e32 v121, v123
	v_permlane32_swap_b32_e32 v124, v126
	v_permlane32_swap_b32_e32 v125, v127
	v_permlane32_swap_b32_e32 v112, v114
	v_permlane32_swap_b32_e32 v113, v115
	v_permlane32_swap_b32_e32 v116, v118
	v_permlane32_swap_b32_e32 v117, v119
	s_add_u32 s24, s34, 0x2380c000
	s_addc_u32 s25, s35, 0
	s_add_u32 s34, s34, 0x2380e000
	s_addc_u32 s35, s35, 0
	s_add_u32 s66, s37, 0x21886000
	s_addc_u32 s67, s64, 0
	v_mov_b32_e32 v168, v200
	v_mov_b32_e32 v169, v201
	global_load_dwordx4 v[176:179], v168, s[24:25]
	global_load_dwordx4 v[172:175], v168, s[34:35]
	s_nop 0
	global_load_dwordx4 v[168:171], v169, s[66:67]
	s_and_b64 vcc, exec, s[2:3]
	s_cbranch_vccnz .LBB4_798
	v_mov_b32_e32 v182, v193
	s_mov_b64 s[2:3], s[8:9]
	global_store_dwordx2 v182, v[184:185], s[2:3] nt

; DI void pv_all_sm(f32x16* o, int vb, bf16x8 pa0, bf16x8 pa1, bf16x8 pa2, bf16x8 pa3, f32x16& p0, f32x16& p1, float& m_ref, f32x16& negm, float& alpha) {
;     ...
;     pv_one<3>(o[3], vb, pa0, pa1, pa2, pa3);
; #pragma unroll
;     for (int r = 0; r < 16; ++r) p0[r] = __builtin_amdgcn_exp2f(p0[r]);
.LBB4_853:
	ds_read_b64_tr_b16 v[214:215], v182 offset:0x600
	ds_read_b64_tr_b16 v[216:217], v182 offset:0xe00
	ds_read_b64_tr_b16 v[218:219], v182 offset:0x1600
	ds_read_b64_tr_b16 v[220:221], v182 offset:0x1e00
	ds_read_b64_tr_b16 v[222:223], v182 offset:0x2600
	ds_read_b64_tr_b16 v[224:225], v182 offset:0x2e00
	ds_read_b64_tr_b16 v[226:227], v182 offset:0x3600
	ds_read_b64_tr_b16 v[228:229], v182 offset:0x3e00
	s_waitcnt lgkmcnt(0)
	s_nop 0
	v_mfma_f32_32x32x16_bf16 v[0:15], v[214:217], v[96:99], v[0:15]
	s_lshl_b32 s2, s57, 14
	s_add_i32 s2, s2, 0
	s_lshl_b32 s3, s57, 13
	v_add_u32_e32 v96, s2, v199
	s_sub_i32 s76, s2, s3
	s_waitcnt vmcnt(0)
	v_add_u32_e32 v97, s2, v200
	v_mfma_f32_32x32x16_bf16 v[0:15], v[218:221], v[108:111], v[0:15]
	s_waitcnt vmcnt(2)
	ds_write_b128 v96, v[176:179]
	v_add_u32_e32 v96, s76, v201
	s_waitcnt vmcnt(1)
	ds_write_b128 v97, v[172:175]
	s_waitcnt vmcnt(0)
	ds_write_b128 v96, v[168:171] offset:49152
	v_cndmask_b32_e64 v96, 0, 1, s[30:31]
	v_cmp_ne_u32_e64 s[2:3], 1, v96
	s_andn2_b64 vcc, exec, s[30:31]
	v_mfma_f32_32x32x16_bf16 v[0:15], v[222:225], v[100:103], v[0:15]
	v_mfma_f32_32x32x16_bf16 v[0:15], v[226:229], v[104:107], v[0:15]
	s_cbranch_vccnz .LBB4_858
	v_mul_f32_e32 v97, 0x44000000, v160
	v_mul_f32_e32 v98, 0x44000000, v164
	v_med3_f32 v97, v97, s56, v210
	v_med3_f32 v98, v98, s56, v210
	v_mov_b32_e32 v99, 0
	v_cvt_pk_fp8_f32 v99, v97, v98
	v_mul_f32_e32 v97, 0x44000000, v161
	v_mul_f32_e32 v98, 0x44000000, v165
	v_med3_f32 v97, v97, s56, v210
	v_med3_f32 v98, v98, s56, v210
	v_mov_b32_e32 v100, 0
	v_cvt_pk_fp8_f32 v100, v97, v98
	v_mul_f32_e32 v97, 0x44000000, v162
	v_mul_f32_e32 v98, 0x44000000, v166
	v_med3_f32 v97, v97, s56, v210
	v_med3_f32 v98, v98, s56, v210
	v_mov_b32_e32 v101, 0
	s_bitcmp1_b32 s58, 0
	v_cvt_pk_fp8_f32 v101, v97, v98
	v_mul_f32_e32 v97, 0x44000000, v163
	v_mul_f32_e32 v98, 0x44000000, v167
	s_cselect_b32 s8, 0x1100, 0
	v_med3_f32 v97, v97, s56, v210
	v_med3_f32 v98, v98, s56, v210
	v_mov_b32_e32 v102, 0
	v_cmp_eq_u32_e32 vcc, 0, v181
	v_add_u32_e32 v96, s8, v190
	v_cvt_pk_fp8_f32 v102, v97, v98
	s_and_b64 vcc, exec, vcc
	s_and_b32 s30, s58, 31
	ds_write_b16 v96, v99
	ds_write_b16 v96, v100 offset:68
	ds_write_b16 v96, v101 offset:136
	ds_write_b16 v96, v102 offset:204
	s_cbranch_vccnz .LBB4_882
	s_lshl_b32 s8, s30, 7
	s_lshl_b32 s9, s58, 6
	s_and_b32 s8, s8, 0xf00
	s_and_b32 s9, s9, 64
	s_or_b32 s26, s8, s9
	s_cbranch_execnz .LBB4_857

; DI void finishSM(f32x16& p0, f32x16& p1, float alpha, float& l_reg, bf16x8& pa0, bf16x8& pa1, bf16x8& pa2, bf16x8& pa3) {
; #pragma unroll
;     for (int r = 0; r < 16; ++r) p1[r] = __builtin_amdgcn_exp2f(p1[r]);
;     float ps = 0;
; #pragma unroll
;     for (int r = 0; r < 16; ++r) ps += p0[r];
; #pragma unroll
;     for (int r = 0; r < 16; ++r) ps += p1[r];
;     { auto rr = __builtin_amdgcn_permlane32_swap(__float_as_uint(ps), __float_as_uint(ps), false, false); ps = __uint_as_float(rr[0]) + __uint_as_float(rr[1]); }
;     l_reg = l_reg * alpha + ps;
;     ...
;     AT_PK4(p0, 0, pa0); AT_PK4(p0, 8, pa1); AT_PK4(p1, 0, pa2); AT_PK4(p1, 8, pa3);
;     ...
; }
; DI void qkt(f32x16& p0, f32x16& p1, const char* Ks, const bf16x8* qr, const f32x16& negm, int r32, int hi) {
; #pragma unroll
;     for (int d0 = 0; d0 < 4; ++d0) { const int cb = (d0 * 16 + hi * 8) * 2;
;         const bf16x8 b0 = *reinterpret_cast<const bf16x8*>(Ks + AT_KSWZ(r32, cb));
;         const bf16x8 b1 = *reinterpret_cast<const bf16x8*>(Ks + AT_KSWZ(32 + r32, cb));
;         p0 = __builtin_amdgcn_mfma_f32_32x32x16_bf16(b0, qr[d0], d0 == 0 ? negm : p0, 0, 0, 0);
;         p1 = __builtin_amdgcn_mfma_f32_32x32x16_bf16(b1, qr[d0], d0 == 0 ? negm : p1, 0, 0, 0); }
; DI void attn_pass(const Frame& F, CvRide& cv, const bf16_t* __restrict__ Qb, const bf16_t* __restrict__ Kh, const bf16_t* __restrict__ Vh, char* lds, f32x16 (&o)[4], float& l_out, const int wave_s) {
;     ...
;     const unsigned cv_ldo = (unsigned)(((tid >> 4) * 2 * 2048 + (tid & 15) * 4) * 4), cv_sto = (unsigned)((tid >> 3) * 2048 + 8 * (tid & 7));
;     const int cv_lw = OFF_CV + (4 * (tid & 15)) * 68 + 2 * (tid >> 4), cv_lr = OFF_CV + (tid >> 3) * 68 + 8 * (tid & 7);
;     f32x4 cvA = f32x4{}, cvB = f32x4{}; unsigned cvr0 = 0, cvr1 = 0;
.LBB4_870:
	v_exp_f32_e32 v182, v128
	v_exp_f32_e32 v230, v129
	v_exp_f32_e32 v231, v130
	v_exp_f32_e32 v232, v131
	v_exp_f32_e32 v233, v132
	v_exp_f32_e32 v234, v133
	v_exp_f32_e32 v235, v134
	v_exp_f32_e32 v236, v135
	v_exp_f32_e32 v237, v136
	v_exp_f32_e32 v238, v137
	v_exp_f32_e32 v239, v138
	v_exp_f32_e32 v240, v139
	v_exp_f32_e32 v241, v140
	v_exp_f32_e32 v242, v141
	v_exp_f32_e32 v243, v142
	v_exp_f32_e32 v244, v143
	v_add_u32_e32 v100, s76, v203
	ds_read_b128 v[96:99], v100 offset:49152
	ds_read_b128 v[168:171], v100 offset:53248
	v_add_u32_e32 v101, s76, v204
	v_add_u32_e32 v102, s76, v205
	v_add_u32_e32 v103, s76, v206
	ds_read_b128 v[172:175], v101 offset:49152
	ds_read_b128 v[176:179], v101 offset:53248
	ds_read_b128 v[214:217], v102 offset:49152
	ds_read_b128 v[218:221], v102 offset:53248
	ds_read_b128 v[222:225], v103 offset:49152
	ds_read_b128 v[226:229], v103 offset:53248
	v_exp_f32_e32 v112, v112
	v_exp_f32_e32 v113, v113
	v_exp_f32_e32 v114, v114
	s_waitcnt lgkmcnt(7)
	v_mfma_f32_32x32x16_bf16 v[128:143], v[96:99], v[156:159], v[64:79]
	v_exp_f32_e32 v115, v115
	v_exp_f32_e32 v116, v116
	v_exp_f32_e32 v117, v117
	v_exp_f32_e32 v118, v118
	v_exp_f32_e32 v119, v119
	s_waitcnt lgkmcnt(6)
	v_mfma_f32_32x32x16_bf16 v[96:111], v[168:171], v[156:159], v[64:79]
	v_exp_f32_e32 v168, v120
	v_add_f32_e32 v120, 0, v182
	v_add_f32_e32 v120, v230, v120
	v_add_f32_e32 v120, v231, v120
	v_add_f32_e32 v120, v232, v120
	v_add_f32_e32 v120, v233, v120
	v_add_f32_e32 v120, v234, v120
	v_add_f32_e32 v120, v235, v120
	v_add_f32_e32 v120, v236, v120
	v_add_f32_e32 v120, v237, v120
	v_add_f32_e32 v120, v238, v120
	s_waitcnt lgkmcnt(5)
	v_mfma_f32_32x32x16_bf16 v[128:143], v[172:175], v[152:155], v[128:143]
	v_add_f32_e32 v120, v239, v120
	v_add_f32_e32 v120, v240, v120
	v_add_f32_e32 v120, v241, v120
	v_add_f32_e32 v120, v242, v120
	v_add_f32_e32 v120, v243, v120
	v_add_f32_e32 v120, v244, v120
	v_add_f32_e32 v120, v112, v120
	s_waitcnt lgkmcnt(4)
	v_mfma_f32_32x32x16_bf16 v[96:111], v[176:179], v[152:155], v[96:111]
	v_add_f32_e32 v120, v113, v120
	v_add_f32_e32 v120, v114, v120
	v_add_f32_e32 v120, v115, v120
	v_add_f32_e32 v120, v116, v120
	v_exp_f32_e32 v169, v121
	v_add_f32_e32 v120, v117, v120
	v_exp_f32_e32 v170, v122
	s_waitcnt lgkmcnt(3)
	v_mfma_f32_32x32x16_bf16 v[128:143], v[214:217], v[148:151], v[128:143]
	v_add_f32_e32 v120, v118, v120
	v_exp_f32_e32 v171, v123
	v_add_f32_e32 v120, v119, v120
	v_exp_f32_e32 v172, v124
	v_add_f32_e32 v120, v168, v120
	v_exp_f32_e32 v173, v125
	v_add_f32_e32 v120, v169, v120
	s_waitcnt lgkmcnt(2)
	v_mfma_f32_32x32x16_bf16 v[96:111], v[218:221], v[148:151], v[96:111]
	v_exp_f32_e32 v174, v126
	v_add_f32_e32 v120, v170, v120
	v_exp_f32_e32 v175, v127
	v_add_f32_e32 v120, v171, v120
	v_add_f32_e32 v120, v172, v120
	v_add_f32_e32 v120, v173, v120
	v_add_f32_e32 v120, v174, v120
	s_waitcnt lgkmcnt(1)
	v_mfma_f32_32x32x16_bf16 v[128:143], v[222:225], v[144:147], v[128:143]
	v_add_f32_e32 v213, v175, v120
	v_mov_b32_e32 v214, v213
	v_cvt_pk_bf16_f32 v120, v182, v230
	v_cvt_pk_bf16_f32 v121, v231, v232
	v_cvt_pk_bf16_f32 v122, v233, v234
	v_cvt_pk_bf16_f32 v123, v235, v236
	v_cvt_pk_bf16_f32 v124, v237, v238
	s_waitcnt lgkmcnt(0)
	v_mfma_f32_32x32x16_bf16 v[96:111], v[226:229], v[144:147], v[96:111]
	v_cvt_pk_bf16_f32 v125, v239, v240
	v_cvt_pk_bf16_f32 v126, v241, v242
	v_cvt_pk_bf16_f32 v127, v243, v244
	v_cvt_pk_bf16_f32 v112, v112, v113
	v_cvt_pk_bf16_f32 v113, v114, v115
	v_cvt_pk_bf16_f32 v114, v116, v117
	v_cvt_pk_bf16_f32 v115, v118, v119
	v_cvt_pk_bf16_f32 v116, v168, v169
	v_cvt_pk_bf16_f32 v117, v170, v171
	v_cvt_pk_bf16_f32 v118, v172, v173
	v_cvt_pk_bf16_f32 v119, v174, v175
	v_permlane32_swap_b32_e32 v213, v214
	v_permlane32_swap_b32_e32 v120, v122
	v_permlane32_swap_b32_e32 v121, v123
	v_permlane32_swap_b32_e32 v124, v126
	v_permlane32_swap_b32_e32 v125, v127
	v_permlane32_swap_b32_e32 v112, v114
	v_permlane32_swap_b32_e32 v113, v115
	v_permlane32_swap_b32_e32 v116, v118
	v_permlane32_swap_b32_e32 v117, v119
	s_add_u32 s34, s66, 0x2380c000
	s_addc_u32 s35, s67, 0
	s_add_u32 s66, s66, 0x2380e000
	s_addc_u32 s67, s67, 0
	s_add_u32 s74, s74, 0x21806000
	s_addc_u32 s75, s75, 0
	v_mov_b32_e32 v168, v197
	v_mov_b32_e32 v169, v196
	global_load_dwordx4 v[176:179], v169, s[34:35]
	global_load_dwordx4 v[172:175], v169, s[66:67]
	s_nop 0
	global_load_dwordx4 v[168:171], v168, s[74:75]
	s_and_b64 vcc, exec, s[2:3]
	s_cbranch_vccnz .LBB4_872
	v_mov_b32_e32 v182, v188
	s_mov_b64 s[2:3], s[8:9]
	global_store_dwordx2 v182, v[184:185], s[2:3] nt

; DI void pv_all_sm(f32x16* o, int vb, bf16x8 pa0, bf16x8 pa1, bf16x8 pa2, bf16x8 pa3, f32x16& p0, f32x16& p1, float& m_ref, f32x16& negm, float& alpha) {
;     ...
;     pv_one<3>(o[3], vb, pa0, pa1, pa2, pa3);
; #pragma unroll
;     for (int r = 0; r < 16; ++r) p0[r] = __builtin_amdgcn_exp2f(p0[r]);
.LBB4_927:
	ds_read_b64_tr_b16 v[218:219], v182 offset:0x600
	ds_read_b64_tr_b16 v[220:221], v182 offset:0xe00
	ds_read_b64_tr_b16 v[222:223], v182 offset:0x1600
	ds_read_b64_tr_b16 v[224:225], v182 offset:0x1e00
	ds_read_b64_tr_b16 v[226:227], v182 offset:0x2600
	ds_read_b64_tr_b16 v[228:229], v182 offset:0x2e00
	ds_read_b64_tr_b16 v[230:231], v182 offset:0x3600
	ds_read_b64_tr_b16 v[232:233], v182 offset:0x3e00
	s_waitcnt lgkmcnt(0)
	s_nop 0
	v_mfma_f32_32x32x16_bf16 v[0:15], v[218:221], v[96:99], v[0:15]
	s_lshl_b32 s2, s15, 14
	s_add_i32 s2, s2, 0
	s_lshl_b32 s3, s15, 13
	v_add_u32_e32 v96, s2, v203
	s_sub_i32 s54, s2, s3
	s_waitcnt vmcnt(0)
	v_add_u32_e32 v97, s2, v204
	v_mfma_f32_32x32x16_bf16 v[0:15], v[222:225], v[108:111], v[0:15]
	s_waitcnt vmcnt(2)
	ds_write_b128 v96, v[176:179]
	v_add_u32_e32 v96, s54, v205
	s_waitcnt vmcnt(1)
	ds_write_b128 v97, v[172:175]
	s_waitcnt vmcnt(0)
	ds_write_b128 v96, v[168:171] offset:49152
	v_cndmask_b32_e64 v96, 0, 1, s[22:23]
	v_cmp_ne_u32_e64 s[2:3], 1, v96
	s_andn2_b64 vcc, exec, s[22:23]
	v_mfma_f32_32x32x16_bf16 v[0:15], v[226:229], v[100:103], v[0:15]
	v_mfma_f32_32x32x16_bf16 v[0:15], v[230:233], v[104:107], v[0:15]
	s_cbranch_vccnz .LBB4_932
	v_mul_f32_e32 v97, 0x44000000, v160
	v_mul_f32_e32 v98, 0x44000000, v164
	v_med3_f32 v97, v97, s28, v214
	v_med3_f32 v98, v98, s28, v214
	v_mov_b32_e32 v99, 0
	v_cvt_pk_fp8_f32 v99, v97, v98
	v_mul_f32_e32 v97, 0x44000000, v161
	v_mul_f32_e32 v98, 0x44000000, v165
	v_med3_f32 v97, v97, s28, v214
	v_med3_f32 v98, v98, s28, v214
	v_mov_b32_e32 v100, 0
	v_cvt_pk_fp8_f32 v100, v97, v98
	v_mul_f32_e32 v97, 0x44000000, v162
	v_mul_f32_e32 v98, 0x44000000, v166
	v_med3_f32 v97, v97, s28, v214
	v_med3_f32 v98, v98, s28, v214
	v_mov_b32_e32 v101, 0
	s_bitcmp1_b32 s58, 0
	v_cvt_pk_fp8_f32 v101, v97, v98
	v_mul_f32_e32 v97, 0x44000000, v163
	v_mul_f32_e32 v98, 0x44000000, v167
	s_cselect_b32 s8, 0x1100, 0
	v_med3_f32 v97, v97, s28, v214
	v_med3_f32 v98, v98, s28, v214
	v_mov_b32_e32 v102, 0
	v_cmp_eq_u32_e32 vcc, 0, v181
	v_add_u32_e32 v96, s8, v195
	v_cvt_pk_fp8_f32 v102, v97, v98
	s_and_b64 vcc, exec, vcc
	s_and_b32 s22, s58, 31
	ds_write_b16 v96, v99
	ds_write_b16 v96, v100 offset:68
	ds_write_b16 v96, v101 offset:136
	ds_write_b16 v96, v102 offset:204
	s_cbranch_vccnz .LBB4_956
	s_lshl_b32 s8, s22, 7
	s_lshl_b32 s9, s58, 6
	s_and_b32 s8, s8, 0xf00
	s_and_b32 s9, s9, 64
	s_or_b32 s18, s8, s9
	s_cbranch_execnz .LBB4_931

; DI void finishSM(f32x16& p0, f32x16& p1, float alpha, float& l_reg, bf16x8& pa0, bf16x8& pa1, bf16x8& pa2, bf16x8& pa3) {
; #pragma unroll
;     for (int r = 0; r < 16; ++r) p1[r] = __builtin_amdgcn_exp2f(p1[r]);
;     float ps = 0;
; #pragma unroll
;     for (int r = 0; r < 16; ++r) ps += p0[r];
; #pragma unroll
;     for (int r = 0; r < 16; ++r) ps += p1[r];
;     { auto rr = __builtin_amdgcn_permlane32_swap(__float_as_uint(ps), __float_as_uint(ps), false, false); ps = __uint_as_float(rr[0]) + __uint_as_float(rr[1]); }
;     l_reg = l_reg * alpha + ps;
;     ...
;     AT_PK4(p0, 0, pa0); AT_PK4(p0, 8, pa1); AT_PK4(p1, 0, pa2); AT_PK4(p1, 8, pa3);
;     ...
; }
; DI void qkt(f32x16& p0, f32x16& p1, const char* Ks, const bf16x8* qr, const f32x16& negm, int r32, int hi) {
; #pragma unroll
;     for (int d0 = 0; d0 < 4; ++d0) { const int cb = (d0 * 16 + hi * 8) * 2;
;         const bf16x8 b0 = *reinterpret_cast<const bf16x8*>(Ks + AT_KSWZ(r32, cb));
;         const bf16x8 b1 = *reinterpret_cast<const bf16x8*>(Ks + AT_KSWZ(32 + r32, cb));
;         p0 = __builtin_amdgcn_mfma_f32_32x32x16_bf16(b0, qr[d0], d0 == 0 ? negm : p0, 0, 0, 0);
;         p1 = __builtin_amdgcn_mfma_f32_32x32x16_bf16(b1, qr[d0], d0 == 0 ? negm : p1, 0, 0, 0); }
; DI void attn_pass(const Frame& F, CvRide& cv, const bf16_t* __restrict__ Qb, const bf16_t* __restrict__ Kh, const bf16_t* __restrict__ Vh, char* lds, f32x16 (&o)[4], float& l_out, const int wave_s) {
;     ...
;     const unsigned cv_ldo = (unsigned)(((tid >> 4) * 2 * 2048 + (tid & 15) * 4) * 4), cv_sto = (unsigned)((tid >> 3) * 2048 + 8 * (tid & 7));
;     const int cv_lw = OFF_CV + (4 * (tid & 15)) * 68 + 2 * (tid >> 4), cv_lr = OFF_CV + (tid >> 3) * 68 + 8 * (tid & 7);
;     f32x4 cvA = f32x4{}, cvB = f32x4{}; unsigned cvr0 = 0, cvr1 = 0;
.LBB4_944:
	v_exp_f32_e32 v182, v128
	v_exp_f32_e32 v234, v129
	v_exp_f32_e32 v235, v130
	v_exp_f32_e32 v236, v131
	v_exp_f32_e32 v237, v132
	v_exp_f32_e32 v238, v133
	v_exp_f32_e32 v239, v134
	v_exp_f32_e32 v240, v135
	v_exp_f32_e32 v241, v136
	v_exp_f32_e32 v242, v137
	v_exp_f32_e32 v243, v138
	v_exp_f32_e32 v244, v139
	v_exp_f32_e32 v245, v140
	v_exp_f32_e32 v246, v141
	v_exp_f32_e32 v247, v142
	v_exp_f32_e32 v248, v143
	v_add_u32_e32 v100, s54, v207
	ds_read_b128 v[96:99], v100 offset:49152
	ds_read_b128 v[168:171], v100 offset:53248
	v_add_u32_e32 v101, s54, v208
	v_add_u32_e32 v102, s54, v209
	v_add_u32_e32 v103, s54, v210
	ds_read_b128 v[172:175], v101 offset:49152
	ds_read_b128 v[176:179], v101 offset:53248
	ds_read_b128 v[218:221], v102 offset:49152
	ds_read_b128 v[222:225], v102 offset:53248
	ds_read_b128 v[226:229], v103 offset:49152
	ds_read_b128 v[230:233], v103 offset:53248
	v_exp_f32_e32 v112, v112
	v_exp_f32_e32 v113, v113
	v_exp_f32_e32 v114, v114
	s_waitcnt lgkmcnt(7)
	v_mfma_f32_32x32x16_bf16 v[128:143], v[96:99], v[156:159], v[64:79]
	v_exp_f32_e32 v115, v115
	v_exp_f32_e32 v116, v116
	v_exp_f32_e32 v117, v117
	v_exp_f32_e32 v118, v118
	v_exp_f32_e32 v119, v119
	s_waitcnt lgkmcnt(6)
	v_mfma_f32_32x32x16_bf16 v[96:111], v[168:171], v[156:159], v[64:79]
	v_exp_f32_e32 v168, v120
	v_add_f32_e32 v120, 0, v182
	v_add_f32_e32 v120, v234, v120
	v_add_f32_e32 v120, v235, v120
	v_add_f32_e32 v120, v236, v120
	v_add_f32_e32 v120, v237, v120
	v_add_f32_e32 v120, v238, v120
	v_add_f32_e32 v120, v239, v120
	v_add_f32_e32 v120, v240, v120
	v_add_f32_e32 v120, v241, v120
	v_add_f32_e32 v120, v242, v120
	s_waitcnt lgkmcnt(5)
	v_mfma_f32_32x32x16_bf16 v[128:143], v[172:175], v[152:155], v[128:143]
	v_add_f32_e32 v120, v243, v120
	v_add_f32_e32 v120, v244, v120
	v_add_f32_e32 v120, v245, v120
	v_add_f32_e32 v120, v246, v120
	v_add_f32_e32 v120, v247, v120
	v_add_f32_e32 v120, v248, v120
	v_add_f32_e32 v120, v112, v120
	s_waitcnt lgkmcnt(4)
	v_mfma_f32_32x32x16_bf16 v[96:111], v[176:179], v[152:155], v[96:111]
	v_add_f32_e32 v120, v113, v120
	v_add_f32_e32 v120, v114, v120
	v_add_f32_e32 v120, v115, v120
	v_add_f32_e32 v120, v116, v120
	v_exp_f32_e32 v169, v121
	v_add_f32_e32 v120, v117, v120
	v_exp_f32_e32 v170, v122
	s_waitcnt lgkmcnt(3)
	v_mfma_f32_32x32x16_bf16 v[128:143], v[218:221], v[148:151], v[128:143]
	v_add_f32_e32 v120, v118, v120
	v_exp_f32_e32 v171, v123
	v_add_f32_e32 v120, v119, v120
	v_exp_f32_e32 v172, v124
	v_add_f32_e32 v120, v168, v120
	v_exp_f32_e32 v173, v125
	v_add_f32_e32 v120, v169, v120
	s_waitcnt lgkmcnt(2)
	v_mfma_f32_32x32x16_bf16 v[96:111], v[222:225], v[148:151], v[96:111]
	v_exp_f32_e32 v174, v126
	v_add_f32_e32 v120, v170, v120
	v_exp_f32_e32 v175, v127
	v_add_f32_e32 v120, v171, v120
	v_add_f32_e32 v120, v172, v120
	v_add_f32_e32 v120, v173, v120
	v_add_f32_e32 v120, v174, v120
	s_waitcnt lgkmcnt(1)
	v_mfma_f32_32x32x16_bf16 v[128:143], v[226:229], v[144:147], v[128:143]
	v_add_f32_e32 v217, v175, v120
	v_mov_b32_e32 v218, v217
	v_cvt_pk_bf16_f32 v120, v182, v234
	v_cvt_pk_bf16_f32 v121, v235, v236
	v_cvt_pk_bf16_f32 v122, v237, v238
	v_cvt_pk_bf16_f32 v123, v239, v240
	v_cvt_pk_bf16_f32 v124, v241, v242
	s_waitcnt lgkmcnt(0)
	v_mfma_f32_32x32x16_bf16 v[96:111], v[230:233], v[144:147], v[96:111]
	v_cvt_pk_bf16_f32 v125, v243, v244
	v_cvt_pk_bf16_f32 v126, v245, v246
	v_cvt_pk_bf16_f32 v127, v247, v248
	v_cvt_pk_bf16_f32 v112, v112, v113
	v_cvt_pk_bf16_f32 v113, v114, v115
	v_cvt_pk_bf16_f32 v114, v116, v117
	v_cvt_pk_bf16_f32 v115, v118, v119
	v_cvt_pk_bf16_f32 v116, v168, v169
	v_cvt_pk_bf16_f32 v117, v170, v171
	v_cvt_pk_bf16_f32 v118, v172, v173
	v_cvt_pk_bf16_f32 v119, v174, v175
	v_permlane32_swap_b32_e32 v217, v218
	v_permlane32_swap_b32_e32 v120, v122
	v_permlane32_swap_b32_e32 v121, v123
	v_permlane32_swap_b32_e32 v124, v126
	v_permlane32_swap_b32_e32 v125, v127
	v_permlane32_swap_b32_e32 v112, v114
	v_permlane32_swap_b32_e32 v113, v115
	v_permlane32_swap_b32_e32 v116, v118
	v_permlane32_swap_b32_e32 v117, v119
	s_add_u32 s24, s34, 0x2380c000
	s_addc_u32 s25, s35, 0
	s_add_u32 s34, s34, 0x2380e000
	s_addc_u32 s35, s35, 0
	s_add_u32 s42, s42, 0x21886000
	s_addc_u32 s43, s43, 0
	v_mov_b32_e32 v168, v201
	v_mov_b32_e32 v169, v200
	global_load_dwordx4 v[176:179], v169, s[24:25]
	global_load_dwordx4 v[172:175], v169, s[34:35]
	s_nop 0
	global_load_dwordx4 v[168:171], v168, s[42:43]
	s_and_b64 vcc, exec, s[2:3]
	s_cbranch_vccnz .LBB4_946
	s_mov_b64 s[2:3], s[8:9]
	v_mov_b32_e32 v182, v193
	global_store_dwordx2 v182, v[184:185], s[2:3] nt

; DI float bflo(unsigned w) { return __uint_as_float(w << 16); }
; DI float bfhi(unsigned w) { return __uint_as_float(w & 0xffff0000u); }
; DI void ph_rowpass(const Frame& F) {
;     ...
;       for (int m = blk * 64 + F.wave * 8; m < blk * 64 + F.wave * 8 + 8; ++m) {
;         const int b = m >> 12, s = m & 4095;
;         const u32x2* mr = (const u32x2*)(MIX + (size_t)m * D) + F.lane;
;         f32x4 v[8]; float ss = 0.f;
; #pragma unroll
;         for (int j = 0; j < 8; ++j) { const u32x2 w = __builtin_nontemporal_load(mr + 64 * j); v[j] = (f32x4){bflo(w.x), bfhi(w.x), bflo(w.y), bfhi(w.y)}; ss += (v[j][0] * v[j][0] + v[j][1] * v[j][1]) + (v[j][2] * v[j][2] + v[j][3] * v[j][3]); }
;         const f32x4* xr = (const f32x4*)(x + (size_t)m * D) + F.lane;
;         f32x4 xc[8];
; #pragma unroll
;         for (int j = 0; j < 8; ++j) xc[j] = __builtin_nontemporal_load(xr + 64 * j);
.LBB4_1120:
	s_lshl_b32 s10, s10, 6
	s_add_i32 s18, s10, s30
	s_add_i32 s19, s18, 8
	s_cmp_ge_i32 s18, s19
	s_waitcnt lgkmcnt(0)
	s_barrier
	s_cbranch_scc1 .LBB4_1117
	s_ashr_i32 s19, s18, 31
	s_add_i32 s10, s31, s10
	s_lshl_b64 s[20:21], s[18:19], 11
	s_and_b32 s10, s10, 0xfff
	v_mov_b32_e32 v59, s21
	v_or_b32_e32 v58, s20, v50
	s_lshl_b64 s[20:21], s[18:19], 13
	s_lshl_b32 s10, s10, 2
	v_lshl_add_u64 v[60:61], v[52:53], 0, s[20:21]
	s_lshl_b64 s[20:21], s[18:19], 12
	v_lshl_add_u64 v[56:57], v[48:49], 0, s[10:11]
	v_mov_b32_e32 v63, s21
	v_or_b32_e32 v62, s20, v54
	s_mov_b64 s[20:21], 0
	s_mov_b32 s92, 0x35800000
	s_mov_b32 s93, 0
	v_lshl_add_u64 v[250:251], s[46:47], 0, v[62:63]
	v_lshl_add_u64 v[252:253], v[60:61], 0, s[20:21]
	v_lshl_add_u64 v[250:251], v[250:251], 0, s[92:93]
	global_load_dwordx2 v[218:219], v[250:251], off nt
	global_load_dwordx2 v[220:221], v[250:251], off offset:512 nt
	global_load_dwordx2 v[222:223], v[250:251], off offset:1024 nt
	global_load_dwordx2 v[224:225], v[250:251], off offset:1536 nt
	global_load_dwordx2 v[226:227], v[250:251], off offset:2048 nt
	global_load_dwordx2 v[228:229], v[250:251], off offset:2560 nt
	global_load_dwordx2 v[230:231], v[250:251], off offset:3072 nt
	global_load_dwordx2 v[232:233], v[250:251], off offset:3584 nt
	global_load_dwordx4 v[234:237], v[252:253], off nt
	global_load_dwordx4 v[238:241], v[252:253], off offset:1024 nt
	global_load_dwordx4 v[242:245], v[252:253], off offset:2048 nt
	global_load_dwordx4 v[246:249], v[252:253], off offset:3072 nt
	global_load_dword v254, v[250:251], off
	s_branch .LBB4_1123

; DI float bflo(unsigned w) { return __uint_as_float(w << 16); }
; DI float bfhi(unsigned w) { return __uint_as_float(w & 0xffff0000u); }
; DI unsigned pk2(float lo, float hi) { unsigned r; asm("v_cvt_pk_bf16_f32 %0, %1, %2" : "=v"(r) : "v"(lo), "v"(hi)); return r; }
; DI void ph_rowpass(const Frame& F) {
;     ...
;       for (int m = blk * 64 + F.wave * 8; m < blk * 64 + F.wave * 8 + 8; ++m) {
;         const int b = m >> 12, s = m & 4095;
;         const u32x2* mr = (const u32x2*)(MIX + (size_t)m * D) + F.lane;
;         f32x4 v[8]; float ss = 0.f;
; #pragma unroll
;         for (int j = 0; j < 8; ++j) { const u32x2 w = __builtin_nontemporal_load(mr + 64 * j); v[j] = (f32x4){bflo(w.x), bfhi(w.x), bflo(w.y), bfhi(w.y)}; ss += (v[j][0] * v[j][0] + v[j][1] * v[j][1]) + (v[j][2] * v[j][2] + v[j][3] * v[j][3]); }
;         const f32x4* xr = (const f32x4*)(x + (size_t)m * D) + F.lane;
;         f32x4 xc[8];
; #pragma unroll
;         for (int j = 0; j < 8; ++j) xc[j] = __builtin_nontemporal_load(xr + 64 * j);
;         const float rstd = rsqrtf(wave_sum(ss) * (1.f / D) + NORM_EPS);
;         u32x2* x1r = (u32x2*)(X1 + (size_t)m * D) + F.lane;
;         float ss2 = 0.f;
; #pragma unroll
;         for (int j = 0; j < 8; ++j) {
;             const f32x4 gg = pgm[F.lane + 64 * j], xv = xc[j];
; #pragma unroll
;             for (int i = 0; i < 4; ++i) v[j][i] = xv[i] + (v[j][i] * rstd) * gg[i];
;             x1r[64 * j] = (u32x2){pk2(v[j][0], v[j][1]), pk2(v[j][2], v[j][3])};
;             ss2 += (v[j][0] * v[j][0] + v[j][1] * v[j][1]) + (v[j][2] * v[j][2] + v[j][3] * v[j][3]);
;         }
;         const float rstd2 = rsqrtf(wave_sum(ss2) * (1.f / D) + NORM_EPS);
.LBB4_1123:
	v_lshl_add_u64 v[12:13], s[46:47], 0, v[62:63]
	v_lshl_add_u64 v[26:27], v[60:61], 0, s[20:21]
	s_waitcnt vmcnt(1)
	v_mov_b64_e32 v[8:9], v[218:219]
	v_mov_b64_e32 v[10:11], v[220:221]
	v_mov_b64_e32 v[14:15], v[222:223]
	v_mov_b64_e32 v[16:17], v[224:225]
	v_mov_b64_e32 v[18:19], v[226:227]
	v_mov_b64_e32 v[20:21], v[228:229]
	v_mov_b64_e32 v[22:23], v[230:231]
	v_mov_b64_e32 v[24:25], v[232:233]
	v_mov_b64_e32 v[32:33], v[234:235]
	v_mov_b64_e32 v[34:35], v[236:237]
	v_mov_b64_e32 v[4:5], v[238:239]
	v_mov_b64_e32 v[6:7], v[240:241]
	v_mov_b64_e32 v[0:1], v[242:243]
	v_mov_b64_e32 v[2:3], v[244:245]
	v_mov_b64_e32 v[28:29], v[246:247]
	v_mov_b64_e32 v[30:31], v[248:249]
	s_waitcnt vmcnt(11)
	v_and_b32_e32 v66, 0xffff0000, v8
	v_and_b32_e32 v70, 0xffff0000, v9
	s_waitcnt vmcnt(10)
	v_and_b32_e32 v158, 0xffff0000, v10
	v_and_b32_e32 v160, 0xffff0000, v11
	v_lshlrev_b32_e32 v64, 16, v8
	v_lshlrev_b32_e32 v68, 16, v9
	v_lshlrev_b32_e32 v153, 16, v10
	v_lshlrev_b32_e32 v159, 16, v11
	s_waitcnt vmcnt(9)
	v_and_b32_e32 v162, 0xffff0000, v14
	v_and_b32_e32 v164, 0xffff0000, v15
	v_mul_f32_e32 v8, v66, v66
	v_mul_f32_e32 v9, v70, v70
	v_mul_f32_e32 v10, v158, v158
	v_mul_f32_e32 v11, v160, v160
	v_lshlrev_b32_e32 v161, 16, v14
	v_lshlrev_b32_e32 v163, 16, v15
	s_waitcnt vmcnt(8)
	v_and_b32_e32 v166, 0xffff0000, v16
	v_and_b32_e32 v168, 0xffff0000, v17
	v_mul_f32_e32 v14, v162, v162
	v_mul_f32_e32 v15, v164, v164
	v_fmac_f32_e32 v8, v64, v64
	v_fmac_f32_e32 v9, v68, v68
	v_fmac_f32_e32 v10, v153, v153
	v_fmac_f32_e32 v11, v159, v159
	v_lshlrev_b32_e32 v165, 16, v16
	v_lshlrev_b32_e32 v167, 16, v17
	s_waitcnt vmcnt(7)
	v_and_b32_e32 v170, 0xffff0000, v18
	v_and_b32_e32 v172, 0xffff0000, v19
	v_mul_f32_e32 v16, v166, v166
	v_mul_f32_e32 v17, v168, v168
	v_fmac_f32_e32 v14, v161, v161
	v_fmac_f32_e32 v15, v163, v163
	v_add_f32_e32 v8, v8, v9
	v_add_f32_e32 v9, v10, v11
	v_lshlrev_b32_e32 v169, 16, v18
	v_lshlrev_b32_e32 v171, 16, v19
	s_waitcnt vmcnt(6)
	v_and_b32_e32 v174, 0xffff0000, v20
	v_and_b32_e32 v176, 0xffff0000, v21
	v_mul_f32_e32 v18, v170, v170
	v_mul_f32_e32 v19, v172, v172
	v_fmac_f32_e32 v16, v165, v165
	v_fmac_f32_e32 v17, v167, v167
	v_add_f32_e32 v10, v14, v15
	v_add_f32_e32 v8, v8, v9
	v_lshlrev_b32_e32 v173, 16, v20
	v_lshlrev_b32_e32 v175, 16, v21
	s_waitcnt vmcnt(5)
	v_and_b32_e32 v178, 0xffff0000, v22
	v_and_b32_e32 v180, 0xffff0000, v23
	v_mul_f32_e32 v20, v174, v174
	v_mul_f32_e32 v21, v176, v176
	v_fmac_f32_e32 v18, v169, v169
	v_fmac_f32_e32 v19, v171, v171
	v_add_f32_e32 v11, v16, v17
	v_add_f32_e32 v8, v8, v10
	v_lshlrev_b32_e32 v177, 16, v22
	v_lshlrev_b32_e32 v179, 16, v23
	s_waitcnt vmcnt(4)
	v_and_b32_e32 v182, 0xffff0000, v24
	v_and_b32_e32 v184, 0xffff0000, v25
	v_mul_f32_e32 v22, v178, v178
	v_mul_f32_e32 v23, v180, v180
	v_fmac_f32_e32 v20, v173, v173
	v_fmac_f32_e32 v21, v175, v175
	v_add_f32_e32 v14, v18, v19
	v_add_f32_e32 v8, v8, v11
	v_lshlrev_b32_e32 v181, 16, v24
	v_lshlrev_b32_e32 v183, 16, v25
	v_mul_f32_e32 v24, v182, v182
	v_fmac_f32_e32 v22, v177, v177
	v_fmac_f32_e32 v23, v179, v179
	v_add_f32_e32 v15, v20, v21
	v_add_f32_e32 v8, v8, v14
	v_mul_f32_e32 v9, v184, v184
	v_fmac_f32_e32 v24, v181, v181
	v_add_f32_e32 v16, v22, v23
	v_add_f32_e32 v8, v8, v15
	v_fmac_f32_e32 v9, v183, v183
	v_add_f32_e32 v8, v8, v16
	v_add_f32_e32 v9, v24, v9
	v_add_f32_e32 v8, v8, v9
	s_nop 1
	v_add_f32_dpp v8, v8, v8 quad_perm:[1,0,3,2] row_mask:0xf bank_mask:0xf bound_ctrl:1
	s_nop 1
	v_add_f32_dpp v8, v8, v8 quad_perm:[2,3,0,1] row_mask:0xf bank_mask:0xf bound_ctrl:1
	s_nop 1
	v_add_f32_dpp v8, v8, v8 row_half_mirror row_mask:0xf bank_mask:0xf bound_ctrl:1
	s_nop 1
	v_add_f32_dpp v10, v8, v8 row_mirror row_mask:0xf bank_mask:0xf bound_ctrl:1
	v_add_co_u32_e32 v8, vcc, s27, v26
	ds_swizzle_b32 v11, v10 offset:swizzle(SWAP,16)
	s_nop 0
	v_addc_co_u32_e32 v9, vcc, 0, v27, vcc
	global_load_dwordx4 v[22:25], v[8:9], off nt
	global_load_dwordx4 v[18:21], v[8:9], off offset:1024 nt
	s_waitcnt lgkmcnt(0)
	v_add_f32_e32 v10, v10, v11
	v_mov_b32_e32 v11, v10
	s_nop 1
	v_permlane32_swap_b32_e32 v10, v11
	v_add_f32_e32 v10, v10, v11
	v_fmamk_f32 v10, v10, 0x3a000000, v151
	v_mul_f32_e32 v11, 0x4b800000, v10
	v_cmp_gt_f32_e32 vcc, s37, v10
	s_nop 1
	v_cndmask_b32_e32 v10, v10, v11, vcc
	v_rsq_f32_e32 v26, v10
	global_load_dwordx4 v[14:17], v[8:9], off offset:2048 nt
	s_nop 0
	global_load_dwordx4 v[8:11], v[8:9], off offset:3072 nt
	ds_read_b128 v[36:39], v67
	ds_read_b128 v[154:157], v67 offset:1024
	v_mul_f32_e32 v27, 0x45800000, v26
	v_cndmask_b32_e32 v185, v26, v27, vcc
	v_mul_f32_e32 v26, v185, v64
	s_waitcnt vmcnt(7) lgkmcnt(1)
	v_fma_f32 v64, v36, v26, v32
	v_mul_f32_e32 v26, v185, v66
	v_fma_f32 v66, v37, v26, v33
	v_mul_f32_e32 v26, v185, v68
	v_fma_f32 v34, v38, v26, v34
	v_mul_f32_e32 v26, v185, v70
	v_fmac_f32_e32 v35, v39, v26
	v_add_co_u32_e32 v32, vcc, s38, v12
	v_mul_f32_e32 v12, v66, v66
	s_nop 0
	v_addc_co_u32_e32 v33, vcc, 0, v13, vcc
	v_mul_f32_e32 v13, v35, v35
	v_fmac_f32_e32 v12, v64, v64
	v_fmac_f32_e32 v13, v34, v34
	v_add_f32_e32 v12, v12, v13
	v_mul_f32_e32 v13, v185, v153
	s_waitcnt vmcnt(6) lgkmcnt(0)
	v_fma_f32 v153, v154, v13, v4
	v_mul_f32_e32 v4, v185, v158
	v_fma_f32 v186, v155, v4, v5
	v_mul_f32_e32 v4, v185, v159
	v_fma_f32 v6, v156, v4, v6
	v_mul_f32_e32 v4, v185, v160
	ds_read_b128 v[36:39], v67 offset:2048
	v_fmac_f32_e32 v7, v157, v4
	v_cvt_pk_bf16_f32 v4, v153, v186
	v_cvt_pk_bf16_f32 v5, v6, v7
	global_store_dwordx2 v[32:33], v[4:5], off offset:512
	v_mul_f32_e32 v4, v186, v186
	v_mul_f32_e32 v5, v7, v7
	v_fmac_f32_e32 v4, v153, v153
	v_fmac_f32_e32 v5, v6, v6
	v_add_f32_e32 v4, v4, v5
	v_mul_f32_e32 v5, v185, v161
	ds_read_b128 v[154:157], v67 offset:3072
	s_waitcnt vmcnt(6) lgkmcnt(1)
; DI unsigned pk2(float lo, float hi) { unsigned r; asm("v_cvt_pk_bf16_f32 %0, %1, %2" : "=v"(r) : "v"(lo), "v"(hi)); return r; }
; DI void ph_rowpass(const Frame& F) {
;     ...
;         for (int j = 0; j < 8; ++j) {
;             const f32x4 gg = pgm[F.lane + 64 * j], xv = xc[j];
; #pragma unroll
;             for (int i = 0; i < 4; ++i) v[j][i] = xv[i] + (v[j][i] * rstd) * gg[i];
;             x1r[64 * j] = (u32x2){pk2(v[j][0], v[j][1]), pk2(v[j][2], v[j][3])};
;             ss2 += (v[j][0] * v[j][0] + v[j][1] * v[j][1]) + (v[j][2] * v[j][2] + v[j][3] * v[j][3]);
;         }
;         const float rstd2 = rsqrtf(wave_sum(ss2) * (1.f / D) + NORM_EPS);
;         u32x2* h2r = (u32x2*)(H2 + (size_t)m * D) + F.lane;
;         f32x2 lgp[8];
; #pragma unroll
;         for (int e = 0; e < 8; ++e) lgp[e] = (f32x2){0.f, 0.f};
; #pragma unroll
;         for (int j = 0; j < 8; ++j) {
;             const f32x4 gg = pgf[F.lane + 64 * j], sh = psh[F.lane + 64 * j];
;             float h[4];
; #pragma unroll
;             for (int i = 0; i < 4; ++i) h[i] = v[j][i] * rstd2 * gg[i] + sh[i];
;     ...
;             ((unsigned*)((unsigned char*)H2 + (size_t)m * D))[F.lane + 64 * j] = pk4_f8(h[0] * F8_HSCALE, h[1] * F8_HSCALE, h[2] * F8_HSCALE, h[3] * F8_HSCALE);
;     ...
;             h2r[64 * j] = (u32x2){pk2(h[0], h[1]), pk2(h[2], h[3])};
	v_fma_f32 v160, v36, v5, v0
	v_mul_f32_e32 v0, v185, v162
	v_fma_f32 v161, v37, v0, v1
	v_mul_f32_e32 v0, v185, v163
	v_fma_f32 v2, v38, v0, v2
	v_mul_f32_e32 v0, v185, v164
	v_fmac_f32_e32 v3, v39, v0
	v_cvt_pk_bf16_f32 v0, v160, v161
	v_cvt_pk_bf16_f32 v1, v2, v3
	global_store_dwordx2 v[32:33], v[0:1], off offset:1024
	v_mul_f32_e32 v0, v161, v161
	v_mul_f32_e32 v1, v3, v3
	v_fmac_f32_e32 v0, v160, v160
	v_fmac_f32_e32 v1, v2, v2
	v_add_f32_e32 v4, v12, v4
	v_add_f32_e32 v0, v0, v1
	v_add_f32_e32 v4, v0, v4
	v_mul_f32_e32 v0, v185, v165
	s_waitcnt vmcnt(6) lgkmcnt(0)
	v_fma_f32 v154, v0, v154, v28
	v_mul_f32_e32 v0, v185, v166
	v_fma_f32 v155, v0, v155, v29
	v_mul_f32_e32 v0, v185, v167
	v_cvt_pk_bf16_f32 v26, v64, v66
	v_cvt_pk_bf16_f32 v27, v34, v35
	v_fma_f32 v156, v0, v156, v30
	v_mul_f32_e32 v0, v185, v168
	global_store_dwordx2 v[32:33], v[26:27], off
	v_fmac_f32_e32 v31, v0, v157
	v_cvt_pk_bf16_f32 v0, v154, v155
	v_cvt_pk_bf16_f32 v1, v156, v31
	ds_read_b128 v[26:29], v67 offset:4096
	ds_read_b128 v[36:39], v67 offset:5120
	global_store_dwordx2 v[32:33], v[0:1], off offset:1536
	v_mul_f32_e32 v0, v155, v155
	v_mul_f32_e32 v1, v31, v31
	v_fmac_f32_e32 v0, v154, v154
	v_fmac_f32_e32 v1, v156, v156
	v_add_f32_e32 v0, v0, v1
	v_add_f32_e32 v4, v4, v0
	v_mul_f32_e32 v0, v185, v169
	s_waitcnt vmcnt(7) lgkmcnt(1)
	v_fma_f32 v22, v0, v26, v22
	v_mul_f32_e32 v0, v185, v170
	v_fma_f32 v23, v0, v27, v23
	v_mul_f32_e32 v0, v185, v171
	v_fma_f32 v157, v0, v28, v24
	v_mul_f32_e32 v0, v185, v172
	v_fmac_f32_e32 v25, v0, v29
	v_cvt_pk_bf16_f32 v0, v22, v23
	v_cvt_pk_bf16_f32 v1, v157, v25
	global_store_dwordx2 v[32:33], v[0:1], off offset:2048
	v_mul_f32_e32 v0, v23, v23
	v_mul_f32_e32 v1, v25, v25
	v_fmac_f32_e32 v0, v22, v22
	v_fmac_f32_e32 v1, v157, v157
	v_add_f32_e32 v0, v0, v1
	v_add_f32_e32 v4, v4, v0
	v_mul_f32_e32 v0, v185, v173
	s_waitcnt vmcnt(7) lgkmcnt(0)
	v_fma_f32 v18, v0, v36, v18
	v_mul_f32_e32 v0, v185, v174
	v_fma_f32 v19, v0, v37, v19
	v_mul_f32_e32 v0, v185, v175
	v_fma_f32 v162, v0, v38, v20
	v_mul_f32_e32 v0, v185, v176
	v_fmac_f32_e32 v21, v0, v39
	v_cvt_pk_bf16_f32 v0, v18, v19
	v_cvt_pk_bf16_f32 v1, v162, v21
	ds_read_b128 v[26:29], v67 offset:6144
	ds_read_b128 v[36:39], v67 offset:7168
	global_store_dwordx2 v[32:33], v[0:1], off offset:2560
	v_mul_f32_e32 v0, v19, v19
	v_mul_f32_e32 v1, v21, v21
	v_fmac_f32_e32 v0, v18, v18
	v_fmac_f32_e32 v1, v162, v162
	v_add_f32_e32 v0, v0, v1
	v_add_f32_e32 v1, v4, v0
	v_mul_f32_e32 v0, v185, v177
	s_waitcnt vmcnt(7) lgkmcnt(1)
	v_fma_f32 v163, v0, v26, v14
	v_mul_f32_e32 v0, v185, v178
	v_fma_f32 v164, v0, v27, v15
	v_mul_f32_e32 v0, v185, v179
	v_fma_f32 v165, v0, v28, v16
	v_mul_f32_e32 v0, v185, v180
	v_fmac_f32_e32 v17, v0, v29
	v_mul_f32_e32 v4, v164, v164
	v_mul_f32_e32 v5, v17, v17
	v_fmac_f32_e32 v4, v163, v163
	v_fmac_f32_e32 v5, v165, v165
	v_add_f32_e32 v4, v4, v5
	v_add_f32_e32 v1, v1, v4
	v_mul_f32_e32 v4, v185, v181
	s_waitcnt vmcnt(6) lgkmcnt(0)
	v_fma_f32 v166, v4, v36, v8
	v_mul_f32_e32 v4, v185, v182
	v_fma_f32 v167, v4, v37, v9
	v_mul_f32_e32 v4, v185, v183
	v_fma_f32 v168, v4, v38, v10
	v_mul_f32_e32 v4, v185, v184
	v_fmac_f32_e32 v11, v4, v39
	v_mul_f32_e32 v4, v167, v167
	v_mul_f32_e32 v5, v11, v11
	v_fmac_f32_e32 v4, v166, v166
	v_fmac_f32_e32 v5, v168, v168
	v_add_f32_e32 v4, v4, v5
	v_add_f32_e32 v1, v1, v4
	v_cvt_pk_bf16_f32 v0, v163, v164
	v_mov_b32_e32 v10, 0
	v_mov_b32_e32 v16, 0
	v_add_f32_dpp v1, v1, v1 quad_perm:[1,0,3,2] row_mask:0xf bank_mask:0xf bound_ctrl:1
	s_nop 1
	v_add_f32_dpp v1, v1, v1 quad_perm:[2,3,0,1] row_mask:0xf bank_mask:0xf bound_ctrl:1
	s_nop 1
	v_add_f32_dpp v1, v1, v1 row_half_mirror row_mask:0xf bank_mask:0xf bound_ctrl:1
	s_nop 1
	v_add_f32_dpp v4, v1, v1 row_mirror row_mask:0xf bank_mask:0xf bound_ctrl:1
	ds_swizzle_b32 v5, v4 offset:swizzle(SWAP,16)
	v_cvt_pk_bf16_f32 v1, v165, v17
	global_store_dwordx2 v[32:33], v[0:1], off offset:3072
	ds_read_b128 v[12:15], v69
	ds_read_b128 v[36:39], v71
	v_cvt_pk_bf16_f32 v0, v166, v167
	s_waitcnt lgkmcnt(2)
	v_add_f32_e32 v4, v4, v5
	v_mov_b32_e32 v5, v4
	s_nop 1
	v_permlane32_swap_b32_e32 v4, v5
	v_add_f32_e32 v4, v4, v5
	v_fmamk_f32 v4, v4, 0x3a000000, v151
	v_mul_f32_e32 v5, 0x4b800000, v4
	v_cmp_gt_f32_e32 vcc, s37, v4
	v_cvt_pk_bf16_f32 v1, v168, v11
	global_store_dwordx2 v[32:33], v[0:1], off offset:3584
	s_nop 0
	v_cndmask_b32_e32 v4, v4, v5, vcc
	v_rsq_f32_e32 v4, v4
	v_mov_b32_e32 v5, 0
	v_mul_f32_e32 v0, 0x45800000, v4
	v_cndmask_b32_e32 v169, v4, v0, vcc
	v_mul_f32_e32 v0, v64, v169
	s_waitcnt lgkmcnt(0)
	v_fma_f32 v202, v12, v0, v36
	v_mul_f32_e32 v0, v66, v169
	v_fma_f32 v70, v13, v0, v37
	v_mul_f32_e32 v0, v34, v169
	v_fma_f32 v68, v14, v0, v38
	v_mul_f32_e32 v0, v35, v169
	v_fmac_f32_e32 v39, v15, v0
	v_mul_f32_e32 v0, 0x41000000, v202
	v_mul_f32_e32 v1, 0x41000000, v70
	v_med3_f32 v0, v0, s39, v152
	v_med3_f32 v1, v1, s39, v152
	v_cvt_pk_fp8_f32 v5, v0, v1
	ds_read_b128 v[12:15], v72
	ds_read_b128 v[32:35], v73
	v_mul_f32_e32 v4, 0x41000000, v68
	v_mul_f32_e32 v0, 0x41000000, v39
	v_med3_f32 v1, v4, s39, v152
	v_med3_f32 v0, v0, s39, v152
	v_cvt_pk_fp8_f32 v5, v1, v0 op_sel:[0,0,1]
	v_lshl_add_u64 v[0:1], s[46:47], 0, v[58:59]
	v_add_co_u32_e32 v158, vcc, s40, v0
	v_mul_f32_e32 v0, v153, v169
	s_waitcnt lgkmcnt(0)
; DI unsigned pk2(float lo, float hi) { unsigned r; asm("v_cvt_pk_bf16_f32 %0, %1, %2" : "=v"(r) : "v"(lo), "v"(hi)); return r; }
; #define RT_LD(W, t_) do { _Pragma("unroll") for (int q = 0; q < 4; ++q) W[q] = wl[((((t_)) * 4 + q) << 6) + F.lane]; } while (0)
; #define RT_FMA(W, t_) do { const float hv_ = v[(t_) >> 2][(t_) & 3]; const f32x2 hh = {hv_, hv_}; _Pragma("unroll") for (int q = 0; q < 4; ++q) { \
;                 lgp[2 * q] = __builtin_elementwise_fma(hh, (f32x2){W[q][0], W[q][1]}, lgp[2 * q]); lgp[2 * q + 1] = __builtin_elementwise_fma(hh, (f32x2){W[q][2], W[q][3]}, lgp[2 * q + 1]); } \
;                 asm volatile("" ::: "memory"); } while (0)
; DI void ph_rowpass(const Frame& F) {
;     ...
;         for (int j = 0; j < 8; ++j) {
;             const f32x4 gg = pgf[F.lane + 64 * j], sh = psh[F.lane + 64 * j];
;             float h[4];
; #pragma unroll
;             for (int i = 0; i < 4; ++i) h[i] = v[j][i] * rstd2 * gg[i] + sh[i];
;     ...
;             ((unsigned*)((unsigned char*)H2 + (size_t)m * D))[F.lane + 64 * j] = pk4_f8(h[0] * F8_HSCALE, h[1] * F8_HSCALE, h[2] * F8_HSCALE, h[3] * F8_HSCALE);
;     ...
;             h2r[64 * j] = (u32x2){pk2(h[0], h[1]), pk2(h[2], h[3])};
;     ...
; #pragma unroll
;             for (int i = 0; i < 4; ++i) v[j][i] = h[i];
;         }
;         {
;             f32x4 wq0[4], wq1[4], wq2[4];
;     ...
;             RT_LD(wq0, 0); RT_LD(wq1, 1);
; #pragma unroll
;             for (int t = 0; t < 30; t += 3) { RT_LD(wq2, t + 2); RT_FMA(wq0, t); RT_LD(wq0, t + 3); RT_FMA(wq1, t + 1); RT_LD(wq1, t + 4); RT_FMA(wq2, t + 2); }
	v_fma_f32 v66, v12, v0, v32
	v_mul_f32_e32 v0, v186, v169
	v_fma_f32 v64, v13, v0, v33
	v_mul_f32_e32 v0, v6, v169
	v_fma_f32 v38, v14, v0, v34
	v_mul_f32_e32 v0, v7, v169
	v_addc_co_u32_e32 v159, vcc, 0, v1, vcc
	v_fmac_f32_e32 v35, v15, v0
	v_mul_f32_e32 v0, 0x41000000, v66
	v_mul_f32_e32 v1, 0x41000000, v64
	global_store_dword v[158:159], v5, off
	v_med3_f32 v0, v0, s39, v152
	v_med3_f32 v1, v1, s39, v152
	v_cvt_pk_fp8_f32 v10, v0, v1
	ds_read_b128 v[4:7], v74
	ds_read_b128 v[26:29], v75
	v_mul_f32_e32 v8, 0x41000000, v38
	v_mul_f32_e32 v9, 0x41000000, v35
	v_med3_f32 v0, v8, s39, v152
	v_med3_f32 v1, v9, s39, v152
	v_cvt_pk_fp8_f32 v10, v0, v1 op_sel:[0,0,1]
	v_mul_f32_e32 v0, v160, v169
	s_waitcnt lgkmcnt(0)
	v_fma_f32 v36, v0, v4, v26
	v_mul_f32_e32 v0, v161, v169
	v_fma_f32 v34, v0, v5, v27
	v_mul_f32_e32 v0, v2, v169
	v_fma_f32 v32, v0, v6, v28
	v_mul_f32_e32 v0, v3, v169
	v_fmac_f32_e32 v29, v0, v7
	v_mul_f32_e32 v0, 0x41000000, v36
	v_mul_f32_e32 v1, 0x41000000, v34
	v_med3_f32 v0, v0, s39, v152
	v_med3_f32 v1, v1, s39, v152
	v_cvt_pk_fp8_f32 v16, v0, v1
	ds_read_b128 v[0:3], v76
	ds_read_b128 v[12:15], v77
	v_mul_f32_e32 v4, 0x41000000, v32
	v_mul_f32_e32 v5, 0x41000000, v29
	v_med3_f32 v4, v4, s39, v152
	v_med3_f32 v5, v5, s39, v152
	v_cvt_pk_fp8_f32 v16, v4, v5 op_sel:[0,0,1]
	v_mul_f32_e32 v4, v154, v169
	s_waitcnt lgkmcnt(0)
	v_fma_f32 v30, v4, v0, v12
	v_mul_f32_e32 v0, v155, v169
	v_fma_f32 v28, v0, v1, v13
	v_mul_f32_e32 v0, v156, v169
	v_fma_f32 v26, v0, v2, v14
	v_mul_f32_e32 v0, v31, v169
	v_fmac_f32_e32 v15, v0, v3
	v_mul_f32_e32 v0, 0x41000000, v30
	v_mul_f32_e32 v1, 0x41000000, v28
	v_med3_f32 v0, v0, s39, v152
	v_med3_f32 v1, v1, s39, v152
	v_mov_b32_e32 v4, 0
	v_cvt_pk_fp8_f32 v4, v0, v1
	v_mul_f32_e32 v2, 0x41000000, v26
	v_mul_f32_e32 v0, 0x41000000, v15
	v_med3_f32 v1, v2, s39, v152
	v_med3_f32 v0, v0, s39, v152
	v_cvt_pk_fp8_f32 v4, v1, v0 op_sel:[0,0,1]
	ds_read_b128 v[0:3], v78
	ds_read_b128 v[6:9], v79
	global_store_dword v[158:159], v10, off offset:256
	global_store_dword v[158:159], v16, off offset:512
	global_store_dword v[158:159], v4, off offset:768
	v_mul_f32_e32 v4, v22, v169
	v_mov_b32_e32 v13, 0
	s_waitcnt lgkmcnt(0)
	v_fma_f32 v24, v4, v0, v6
	v_mul_f32_e32 v0, v23, v169
	v_fma_f32 v22, v0, v1, v7
	v_mul_f32_e32 v0, v157, v169
	v_fma_f32 v20, v0, v2, v8
	v_mul_f32_e32 v0, v25, v169
	v_fmac_f32_e32 v9, v0, v3
	v_mul_f32_e32 v0, 0x41000000, v24
	v_mul_f32_e32 v1, 0x41000000, v22
	v_med3_f32 v0, v0, s39, v152
	v_med3_f32 v1, v1, s39, v152
	v_cvt_pk_fp8_f32 v13, v0, v1
	ds_read_b128 v[0:3], v80
	ds_read_b128 v[4:7], v81
	v_mul_f32_e32 v8, 0x41000000, v20
	v_mul_f32_e32 v10, 0x41000000, v9
	v_med3_f32 v8, v8, s39, v152
	v_med3_f32 v10, v10, s39, v152
	v_cvt_pk_fp8_f32 v13, v8, v10 op_sel:[0,0,1]
	v_mul_f32_e32 v8, v18, v169
	s_waitcnt lgkmcnt(0)
	v_fma_f32 v18, v8, v0, v4
	v_mul_f32_e32 v0, v19, v169
	v_fma_f32 v16, v0, v1, v5
	v_mul_f32_e32 v0, v162, v169
	v_fma_f32 v14, v0, v2, v6
	v_mul_f32_e32 v0, v21, v169
	v_fmac_f32_e32 v7, v0, v3
	v_mul_f32_e32 v0, 0x41000000, v18
	v_mul_f32_e32 v1, 0x41000000, v16
	v_med3_f32 v0, v0, s39, v152
	v_med3_f32 v1, v1, s39, v152
	v_mov_b32_e32 v19, 0
	v_cvt_pk_fp8_f32 v19, v0, v1
	ds_read_b128 v[154:157], v82
	ds_read_b128 v[2:5], v83
	v_mul_f32_e32 v6, 0x41000000, v14
	v_mul_f32_e32 v8, 0x41000000, v7
	v_med3_f32 v0, v6, s39, v152
	v_med3_f32 v1, v8, s39, v152
	v_cvt_pk_fp8_f32 v19, v0, v1 op_sel:[0,0,1]
	v_mul_f32_e32 v0, v163, v169
	s_waitcnt lgkmcnt(0)
	v_fma_f32 v12, v0, v154, v2
	v_mul_f32_e32 v0, v164, v169
	v_fma_f32 v10, v0, v155, v3
	v_mul_f32_e32 v0, v165, v169
	v_fma_f32 v8, v0, v156, v4
	v_mul_f32_e32 v0, v17, v169
	v_fmac_f32_e32 v5, v0, v157
	v_mul_f32_e32 v0, 0x41000000, v12
	v_mul_f32_e32 v1, 0x41000000, v10
	v_med3_f32 v0, v0, s39, v152
	v_med3_f32 v1, v1, s39, v152
	v_mov_b32_e32 v17, 0
	v_cvt_pk_fp8_f32 v17, v0, v1
	ds_read_b128 v[154:157], v84
	ds_read_b128 v[0:3], v85
	v_mul_f32_e32 v4, 0x41000000, v8
	v_mul_f32_e32 v6, 0x41000000, v5
	v_med3_f32 v4, v4, s39, v152
	v_med3_f32 v6, v6, s39, v152
	v_cvt_pk_fp8_f32 v17, v4, v6 op_sel:[0,0,1]
	v_mul_f32_e32 v4, v166, v169
	s_waitcnt lgkmcnt(0)
	v_fma_f32 v6, v4, v154, v0
	v_mul_f32_e32 v0, v167, v169
	v_fma_f32 v4, v0, v155, v1
	v_mul_f32_e32 v0, v168, v169
	v_mul_f32_e32 v1, v11, v169
	v_fma_f32 v0, v0, v156, v2
	v_fmac_f32_e32 v3, v1, v157
	v_mul_f32_e32 v1, 0x41000000, v6
	v_mul_f32_e32 v2, 0x41000000, v4
	v_med3_f32 v1, v1, s39, v152
	v_med3_f32 v2, v2, s39, v152
	v_mov_b32_e32 v21, 0
	v_cvt_pk_fp8_f32 v21, v1, v2
	v_mul_f32_e32 v11, 0x41000000, v0
	v_mul_f32_e32 v1, 0x41000000, v3
	v_med3_f32 v2, v11, s39, v152
	v_med3_f32 v1, v1, s39, v152
	v_cvt_pk_fp8_f32 v21, v2, v1 op_sel:[0,0,1]
	global_store_dword v[158:159], v13, off offset:1024
	global_store_dword v[158:159], v19, off offset:1280
	global_store_dword v[158:159], v17, off offset:1536
	global_store_dword v[158:159], v21, off offset:1792
	s_cmp_eq_u32 s20, 0xe000
	s_cselect_b32 s92, 0, 0x1000
	s_cselect_b32 s94, 0, 0x2000
	s_mov_b32 s93, 0
	s_mov_b32 s95, 0
	v_lshl_add_u64 v[250:251], s[46:47], 0, v[62:63]
	v_lshl_add_u64 v[252:253], v[60:61], 0, s[20:21]
	v_lshl_add_u64 v[250:251], v[250:251], 0, s[92:93]
	v_lshl_add_u64 v[252:253], v[252:253], 0, s[94:95]
	s_mov_b32 s92, 0x35800000
	s_nop 0
	v_lshl_add_u64 v[250:251], v[250:251], 0, s[92:93]
	global_load_dwordx2 v[218:219], v[250:251], off nt
	global_load_dwordx2 v[220:221], v[250:251], off offset:512 nt
	global_load_dwordx2 v[222:223], v[250:251], off offset:1024 nt
	global_load_dwordx2 v[224:225], v[250:251], off offset:1536 nt
	global_load_dwordx2 v[226:227], v[250:251], off offset:2048 nt
	global_load_dwordx2 v[228:229], v[250:251], off offset:2560 nt
	global_load_dwordx2 v[230:231], v[250:251], off offset:3072 nt
	global_load_dwordx2 v[232:233], v[250:251], off offset:3584 nt
	global_load_dwordx4 v[234:237], v[252:253], off nt
	global_load_dwordx4 v[238:241], v[252:253], off offset:1024 nt
	global_load_dwordx4 v[242:245], v[252:253], off offset:2048 nt
	global_load_dwordx4 v[246:249], v[252:253], off offset:3072 nt
	ds_read_b128 v[154:157], v86
	ds_read_b128 v[158:161], v86 offset:1024
	ds_read_b128 v[162:165], v86 offset:2048
	ds_read_b128 v[166:169], v86 offset:3072
	ds_read_b128 v[170:173], v86 offset:4096
	ds_read_b128 v[174:177], v86 offset:5120
	ds_read_b128 v[178:181], v86 offset:6144
	ds_read_b128 v[182:185], v86 offset:7168
	ds_read_b128 v[186:189], v86 offset:8192
	ds_read_b128 v[190:193], v86 offset:9216
	ds_read_b128 v[194:197], v86 offset:10240
	ds_read_b128 v[198:201], v86 offset:11264
	s_waitcnt lgkmcnt(11)
; #define RT_LD(W, t_) do { _Pragma("unroll") for (int q = 0; q < 4; ++q) W[q] = wl[((((t_)) * 4 + q) << 6) + F.lane]; } while (0)
; #define RT_FMA(W, t_) do { const float hv_ = v[(t_) >> 2][(t_) & 3]; const f32x2 hh = {hv_, hv_}; _Pragma("unroll") for (int q = 0; q < 4; ++q) { \
;                 lgp[2 * q] = __builtin_elementwise_fma(hh, (f32x2){W[q][0], W[q][1]}, lgp[2 * q]); lgp[2 * q + 1] = __builtin_elementwise_fma(hh, (f32x2){W[q][2], W[q][3]}, lgp[2 * q + 1]); } \
;                 asm volatile("" ::: "memory"); } while (0)
; DI void ph_rowpass(const Frame& F) {
;     ...
;             f32x4 wq0[4], wq1[4], wq2[4];
;     ...
;             RT_LD(wq0, 0); RT_LD(wq1, 1);
; #pragma unroll
;             for (int t = 0; t < 30; t += 3) { RT_LD(wq2, t + 2); RT_FMA(wq0, t); RT_LD(wq0, t + 3); RT_FMA(wq1, t + 1); RT_LD(wq1, t + 4); RT_FMA(wq2, t + 2); }
;             RT_FMA(wq0, 30); RT_FMA(wq1, 31);
	v_pk_fma_f32 v[204:205], v[202:203], v[154:155], 0 op_sel_hi:[0,1,0]
	v_pk_fma_f32 v[206:207], v[202:203], v[156:157], 0 op_sel_hi:[0,1,0]
	s_waitcnt lgkmcnt(10)
	v_pk_fma_f32 v[208:209], v[202:203], v[158:159], 0 op_sel_hi:[0,1,0]
	v_pk_fma_f32 v[210:211], v[202:203], v[160:161], 0 op_sel_hi:[0,1,0]
	s_waitcnt lgkmcnt(9)
	v_pk_fma_f32 v[212:213], v[202:203], v[162:163], 0 op_sel_hi:[0,1,0]
	v_pk_fma_f32 v[214:215], v[202:203], v[164:165], 0 op_sel_hi:[0,1,0]
	s_waitcnt lgkmcnt(8)
	v_pk_fma_f32 v[216:217], v[202:203], v[166:167], 0 op_sel_hi:[0,1,0]
	v_pk_fma_f32 v[202:203], v[202:203], v[168:169], 0 op_sel_hi:[0,1,0]
	ds_read_b128 v[154:157], v86 offset:12288
	ds_read_b128 v[158:161], v86 offset:13312
	ds_read_b128 v[162:165], v86 offset:14336
	ds_read_b128 v[166:169], v86 offset:15360
	s_waitcnt lgkmcnt(11)
	v_pk_fma_f32 v[204:205], v[70:71], v[170:171], v[204:205] op_sel_hi:[0,1,1]
	v_pk_fma_f32 v[206:207], v[70:71], v[172:173], v[206:207] op_sel_hi:[0,1,1]
	s_waitcnt lgkmcnt(10)
	v_pk_fma_f32 v[208:209], v[70:71], v[174:175], v[208:209] op_sel_hi:[0,1,1]
	v_pk_fma_f32 v[210:211], v[70:71], v[176:177], v[210:211] op_sel_hi:[0,1,1]
	s_waitcnt lgkmcnt(9)
	v_pk_fma_f32 v[212:213], v[70:71], v[178:179], v[212:213] op_sel_hi:[0,1,1]
	v_pk_fma_f32 v[214:215], v[70:71], v[180:181], v[214:215] op_sel_hi:[0,1,1]
	s_waitcnt lgkmcnt(8)
	v_pk_fma_f32 v[216:217], v[70:71], v[182:183], v[216:217] op_sel_hi:[0,1,1]
	v_pk_fma_f32 v[202:203], v[70:71], v[184:185], v[202:203] op_sel_hi:[0,1,1]
	ds_read_b128 v[170:173], v86 offset:16384
	ds_read_b128 v[174:177], v86 offset:17408
	ds_read_b128 v[178:181], v86 offset:18432
	ds_read_b128 v[182:185], v86 offset:19456
	s_waitcnt lgkmcnt(11)
	v_pk_fma_f32 v[204:205], v[68:69], v[186:187], v[204:205] op_sel_hi:[0,1,1]
	v_pk_fma_f32 v[206:207], v[68:69], v[188:189], v[206:207] op_sel_hi:[0,1,1]
	s_waitcnt lgkmcnt(10)
	v_pk_fma_f32 v[208:209], v[68:69], v[190:191], v[208:209] op_sel_hi:[0,1,1]
	v_pk_fma_f32 v[210:211], v[68:69], v[192:193], v[210:211] op_sel_hi:[0,1,1]
	s_waitcnt lgkmcnt(9)
	v_pk_fma_f32 v[212:213], v[68:69], v[194:195], v[212:213] op_sel_hi:[0,1,1]
	v_pk_fma_f32 v[214:215], v[68:69], v[196:197], v[214:215] op_sel_hi:[0,1,1]
	s_waitcnt lgkmcnt(8)
	v_pk_fma_f32 v[216:217], v[68:69], v[198:199], v[216:217] op_sel_hi:[0,1,1]
	v_pk_fma_f32 v[202:203], v[68:69], v[200:201], v[202:203] op_sel_hi:[0,1,1]
	ds_read_b128 v[186:189], v86 offset:20480
	ds_read_b128 v[190:193], v86 offset:21504
	ds_read_b128 v[194:197], v86 offset:22528
	ds_read_b128 v[198:201], v86 offset:23552
	v_mov_b32_e32 v2, v39
	s_waitcnt lgkmcnt(11)
	v_pk_fma_f32 v[204:205], v[2:3], v[154:155], v[204:205] op_sel_hi:[0,1,1]
	v_pk_fma_f32 v[206:207], v[2:3], v[156:157], v[206:207] op_sel_hi:[0,1,1]
	s_waitcnt lgkmcnt(10)
	v_pk_fma_f32 v[208:209], v[2:3], v[158:159], v[208:209] op_sel_hi:[0,1,1]
	v_pk_fma_f32 v[210:211], v[2:3], v[160:161], v[210:211] op_sel_hi:[0,1,1]
	s_waitcnt lgkmcnt(9)
	v_pk_fma_f32 v[212:213], v[2:3], v[162:163], v[212:213] op_sel_hi:[0,1,1]
	v_pk_fma_f32 v[214:215], v[2:3], v[164:165], v[214:215] op_sel_hi:[0,1,1]
	s_waitcnt lgkmcnt(8)
	v_pk_fma_f32 v[216:217], v[2:3], v[166:167], v[216:217] op_sel_hi:[0,1,1]
	v_pk_fma_f32 v[202:203], v[2:3], v[168:169], v[202:203] op_sel_hi:[0,1,1]
	ds_read_b128 v[154:157], v86 offset:24576
	ds_read_b128 v[158:161], v86 offset:25600
	ds_read_b128 v[162:165], v86 offset:26624
	ds_read_b128 v[166:169], v86 offset:27648
	s_waitcnt lgkmcnt(11)
	v_pk_fma_f32 v[204:205], v[66:67], v[170:171], v[204:205] op_sel_hi:[0,1,1]
	v_pk_fma_f32 v[206:207], v[66:67], v[172:173], v[206:207] op_sel_hi:[0,1,1]
	s_waitcnt lgkmcnt(10)
	v_pk_fma_f32 v[208:209], v[66:67], v[174:175], v[208:209] op_sel_hi:[0,1,1]
	v_pk_fma_f32 v[210:211], v[66:67], v[176:177], v[210:211] op_sel_hi:[0,1,1]
	s_waitcnt lgkmcnt(9)
	v_pk_fma_f32 v[212:213], v[66:67], v[178:179], v[212:213] op_sel_hi:[0,1,1]
	v_pk_fma_f32 v[214:215], v[66:67], v[180:181], v[214:215] op_sel_hi:[0,1,1]
	s_waitcnt lgkmcnt(8)
	v_pk_fma_f32 v[216:217], v[66:67], v[182:183], v[216:217] op_sel_hi:[0,1,1]
	v_pk_fma_f32 v[202:203], v[66:67], v[184:185], v[202:203] op_sel_hi:[0,1,1]
	ds_read_b128 v[170:173], v86 offset:28672
	ds_read_b128 v[174:177], v86 offset:29696
	ds_read_b128 v[178:181], v86 offset:30720
	ds_read_b128 v[182:185], v86 offset:31744
	s_waitcnt lgkmcnt(11)
	v_pk_fma_f32 v[204:205], v[64:65], v[186:187], v[204:205] op_sel_hi:[0,1,1]
	v_pk_fma_f32 v[206:207], v[64:65], v[188:189], v[206:207] op_sel_hi:[0,1,1]
	s_waitcnt lgkmcnt(10)
	v_pk_fma_f32 v[208:209], v[64:65], v[190:191], v[208:209] op_sel_hi:[0,1,1]
	v_pk_fma_f32 v[210:211], v[64:65], v[192:193], v[210:211] op_sel_hi:[0,1,1]
	s_waitcnt lgkmcnt(9)
	v_pk_fma_f32 v[212:213], v[64:65], v[194:195], v[212:213] op_sel_hi:[0,1,1]
	v_pk_fma_f32 v[214:215], v[64:65], v[196:197], v[214:215] op_sel_hi:[0,1,1]
	s_waitcnt lgkmcnt(8)
	v_pk_fma_f32 v[216:217], v[64:65], v[198:199], v[216:217] op_sel_hi:[0,1,1]
	v_pk_fma_f32 v[202:203], v[64:65], v[200:201], v[202:203] op_sel_hi:[0,1,1]
	ds_read_b128 v[186:189], v86 offset:32768
	ds_read_b128 v[190:193], v86 offset:33792
	ds_read_b128 v[194:197], v86 offset:34816
	ds_read_b128 v[198:201], v86 offset:35840
	s_waitcnt lgkmcnt(11)
	v_pk_fma_f32 v[204:205], v[38:39], v[154:155], v[204:205] op_sel_hi:[0,1,1]
	v_pk_fma_f32 v[206:207], v[38:39], v[156:157], v[206:207] op_sel_hi:[0,1,1]
	s_waitcnt lgkmcnt(10)
	v_pk_fma_f32 v[208:209], v[38:39], v[158:159], v[208:209] op_sel_hi:[0,1,1]
	v_pk_fma_f32 v[210:211], v[38:39], v[160:161], v[210:211] op_sel_hi:[0,1,1]
	s_waitcnt lgkmcnt(9)
; #define RT_LD(W, t_) do { _Pragma("unroll") for (int q = 0; q < 4; ++q) W[q] = wl[((((t_)) * 4 + q) << 6) + F.lane]; } while (0)
; #define RT_FMA(W, t_) do { const float hv_ = v[(t_) >> 2][(t_) & 3]; const f32x2 hh = {hv_, hv_}; _Pragma("unroll") for (int q = 0; q < 4; ++q) { \
;                 lgp[2 * q] = __builtin_elementwise_fma(hh, (f32x2){W[q][0], W[q][1]}, lgp[2 * q]); lgp[2 * q + 1] = __builtin_elementwise_fma(hh, (f32x2){W[q][2], W[q][3]}, lgp[2 * q + 1]); } \
;                 asm volatile("" ::: "memory"); } while (0)
; DI void ph_rowpass(const Frame& F) {
;     ...
;             f32x4 wq0[4], wq1[4], wq2[4];
;     ...
;             RT_LD(wq0, 0); RT_LD(wq1, 1);
; #pragma unroll
;             for (int t = 0; t < 30; t += 3) { RT_LD(wq2, t + 2); RT_FMA(wq0, t); RT_LD(wq0, t + 3); RT_FMA(wq1, t + 1); RT_LD(wq1, t + 4); RT_FMA(wq2, t + 2); }
;             RT_FMA(wq0, 30); RT_FMA(wq1, 31);
	v_pk_fma_f32 v[212:213], v[38:39], v[162:163], v[212:213] op_sel_hi:[0,1,1]
	v_pk_fma_f32 v[214:215], v[38:39], v[164:165], v[214:215] op_sel_hi:[0,1,1]
	s_waitcnt lgkmcnt(8)
	v_pk_fma_f32 v[216:217], v[38:39], v[166:167], v[216:217] op_sel_hi:[0,1,1]
	v_pk_fma_f32 v[38:39], v[38:39], v[168:169], v[202:203] op_sel_hi:[0,1,1]
	ds_read_b128 v[154:157], v86 offset:36864
	ds_read_b128 v[158:161], v86 offset:37888
	ds_read_b128 v[162:165], v86 offset:38912
	ds_read_b128 v[166:169], v86 offset:39936
	v_mov_b32_e32 v2, v35
	s_waitcnt lgkmcnt(11)
	v_pk_fma_f32 v[202:203], v[2:3], v[170:171], v[204:205] op_sel_hi:[0,1,1]
	v_pk_fma_f32 v[204:205], v[2:3], v[172:173], v[206:207] op_sel_hi:[0,1,1]
	s_waitcnt lgkmcnt(10)
	v_pk_fma_f32 v[206:207], v[2:3], v[174:175], v[208:209] op_sel_hi:[0,1,1]
	v_pk_fma_f32 v[208:209], v[2:3], v[176:177], v[210:211] op_sel_hi:[0,1,1]
	s_waitcnt lgkmcnt(9)
	v_pk_fma_f32 v[210:211], v[2:3], v[178:179], v[212:213] op_sel_hi:[0,1,1]
	v_pk_fma_f32 v[212:213], v[2:3], v[180:181], v[214:215] op_sel_hi:[0,1,1]
	s_waitcnt lgkmcnt(8)
	v_pk_fma_f32 v[214:215], v[2:3], v[182:183], v[216:217] op_sel_hi:[0,1,1]
	v_pk_fma_f32 v[38:39], v[2:3], v[184:185], v[38:39] op_sel_hi:[0,1,1]
	ds_read_b128 v[170:173], v86 offset:40960
	ds_read_b128 v[174:177], v86 offset:41984
	ds_read_b128 v[178:181], v86 offset:43008
	ds_read_b128 v[182:185], v86 offset:44032
	s_waitcnt lgkmcnt(11)
	v_pk_fma_f32 v[202:203], v[36:37], v[186:187], v[202:203] op_sel_hi:[0,1,1]
	v_pk_fma_f32 v[204:205], v[36:37], v[188:189], v[204:205] op_sel_hi:[0,1,1]
	s_waitcnt lgkmcnt(10)
	v_pk_fma_f32 v[206:207], v[36:37], v[190:191], v[206:207] op_sel_hi:[0,1,1]
	v_pk_fma_f32 v[208:209], v[36:37], v[192:193], v[208:209] op_sel_hi:[0,1,1]
	s_waitcnt lgkmcnt(9)
	v_pk_fma_f32 v[210:211], v[36:37], v[194:195], v[210:211] op_sel_hi:[0,1,1]
	v_pk_fma_f32 v[212:213], v[36:37], v[196:197], v[212:213] op_sel_hi:[0,1,1]
	s_waitcnt lgkmcnt(8)
	v_pk_fma_f32 v[198:199], v[36:37], v[198:199], v[214:215] op_sel_hi:[0,1,1]
	v_pk_fma_f32 v[200:201], v[36:37], v[200:201], v[38:39] op_sel_hi:[0,1,1]
	ds_read_b128 v[36:39], v86 offset:45056
	ds_read_b128 v[186:189], v86 offset:46080
	ds_read_b128 v[190:193], v86 offset:47104
	ds_read_b128 v[194:197], v86 offset:48128
	s_waitcnt lgkmcnt(11)
	v_pk_fma_f32 v[202:203], v[34:35], v[154:155], v[202:203] op_sel_hi:[0,1,1]
	v_pk_fma_f32 v[204:205], v[34:35], v[156:157], v[204:205] op_sel_hi:[0,1,1]
	s_waitcnt lgkmcnt(10)
	v_pk_fma_f32 v[206:207], v[34:35], v[158:159], v[206:207] op_sel_hi:[0,1,1]
	v_pk_fma_f32 v[208:209], v[34:35], v[160:161], v[208:209] op_sel_hi:[0,1,1]
	s_waitcnt lgkmcnt(9)
	v_pk_fma_f32 v[210:211], v[34:35], v[162:163], v[210:211] op_sel_hi:[0,1,1]
	v_pk_fma_f32 v[212:213], v[34:35], v[164:165], v[212:213] op_sel_hi:[0,1,1]
	s_waitcnt lgkmcnt(8)
	v_pk_fma_f32 v[198:199], v[34:35], v[166:167], v[198:199] op_sel_hi:[0,1,1]
	v_pk_fma_f32 v[34:35], v[34:35], v[168:169], v[200:201] op_sel_hi:[0,1,1]
	ds_read_b128 v[154:157], v86 offset:49152
	ds_read_b128 v[158:161], v86 offset:50176
	ds_read_b128 v[162:165], v86 offset:51200
	ds_read_b128 v[166:169], v86 offset:52224
	s_waitcnt lgkmcnt(11)
	v_pk_fma_f32 v[200:201], v[32:33], v[170:171], v[202:203] op_sel_hi:[0,1,1]
	v_pk_fma_f32 v[202:203], v[32:33], v[172:173], v[204:205] op_sel_hi:[0,1,1]
	s_waitcnt lgkmcnt(10)
	v_pk_fma_f32 v[204:205], v[32:33], v[174:175], v[206:207] op_sel_hi:[0,1,1]
	v_pk_fma_f32 v[206:207], v[32:33], v[176:177], v[208:209] op_sel_hi:[0,1,1]
	s_waitcnt lgkmcnt(9)
	v_pk_fma_f32 v[208:209], v[32:33], v[178:179], v[210:211] op_sel_hi:[0,1,1]
	v_pk_fma_f32 v[210:211], v[32:33], v[180:181], v[212:213] op_sel_hi:[0,1,1]
	s_waitcnt lgkmcnt(8)
	v_pk_fma_f32 v[182:183], v[32:33], v[182:183], v[198:199] op_sel_hi:[0,1,1]
	v_pk_fma_f32 v[184:185], v[32:33], v[184:185], v[34:35] op_sel_hi:[0,1,1]
	ds_read_b128 v[32:35], v86 offset:53248
	ds_read_b128 v[170:173], v86 offset:54272
	ds_read_b128 v[174:177], v86 offset:55296
	ds_read_b128 v[178:181], v86 offset:56320
	v_mov_b32_e32 v2, v29
	s_waitcnt lgkmcnt(11)
	v_pk_fma_f32 v[198:199], v[2:3], v[36:37], v[200:201] op_sel_hi:[0,1,1]
	v_pk_fma_f32 v[200:201], v[2:3], v[38:39], v[202:203] op_sel_hi:[0,1,1]
	s_waitcnt lgkmcnt(10)
	v_pk_fma_f32 v[202:203], v[2:3], v[186:187], v[204:205] op_sel_hi:[0,1,1]
	v_pk_fma_f32 v[204:205], v[2:3], v[188:189], v[206:207] op_sel_hi:[0,1,1]
	s_waitcnt lgkmcnt(9)
	v_pk_fma_f32 v[206:207], v[2:3], v[190:191], v[208:209] op_sel_hi:[0,1,1]
	v_pk_fma_f32 v[208:209], v[2:3], v[192:193], v[210:211] op_sel_hi:[0,1,1]
	s_waitcnt lgkmcnt(8)
	v_pk_fma_f32 v[194:195], v[2:3], v[194:195], v[182:183] op_sel_hi:[0,1,1]
	v_pk_fma_f32 v[196:197], v[2:3], v[196:197], v[184:185] op_sel_hi:[0,1,1]
	ds_read_b128 v[36:39], v86 offset:57344
	ds_read_b128 v[182:185], v86 offset:58368
	ds_read_b128 v[186:189], v86 offset:59392
	ds_read_b128 v[190:193], v86 offset:60416
	s_waitcnt lgkmcnt(11)
	v_pk_fma_f32 v[198:199], v[30:31], v[154:155], v[198:199] op_sel_hi:[0,1,1]
	v_pk_fma_f32 v[200:201], v[30:31], v[156:157], v[200:201] op_sel_hi:[0,1,1]
	s_waitcnt lgkmcnt(10)
	v_pk_fma_f32 v[202:203], v[30:31], v[158:159], v[202:203] op_sel_hi:[0,1,1]
	v_pk_fma_f32 v[204:205], v[30:31], v[160:161], v[204:205] op_sel_hi:[0,1,1]
	s_waitcnt lgkmcnt(9)
	v_pk_fma_f32 v[206:207], v[30:31], v[162:163], v[206:207] op_sel_hi:[0,1,1]
	v_pk_fma_f32 v[208:209], v[30:31], v[164:165], v[208:209] op_sel_hi:[0,1,1]
	s_waitcnt lgkmcnt(8)
	v_pk_fma_f32 v[194:195], v[30:31], v[166:167], v[194:195] op_sel_hi:[0,1,1]
	v_pk_fma_f32 v[30:31], v[30:31], v[168:169], v[196:197] op_sel_hi:[0,1,1]
	ds_read_b128 v[154:157], v86 offset:61440
	ds_read_b128 v[158:161], v86 offset:62464
	ds_read_b128 v[162:165], v86 offset:63488
	ds_read_b128 v[166:169], v86 offset:64512
	s_waitcnt lgkmcnt(11)
; #define RT_LD(W, t_) do { _Pragma("unroll") for (int q = 0; q < 4; ++q) W[q] = wl[((((t_)) * 4 + q) << 6) + F.lane]; } while (0)
; #define RT_FMA(W, t_) do { const float hv_ = v[(t_) >> 2][(t_) & 3]; const f32x2 hh = {hv_, hv_}; _Pragma("unroll") for (int q = 0; q < 4; ++q) { \
;                 lgp[2 * q] = __builtin_elementwise_fma(hh, (f32x2){W[q][0], W[q][1]}, lgp[2 * q]); lgp[2 * q + 1] = __builtin_elementwise_fma(hh, (f32x2){W[q][2], W[q][3]}, lgp[2 * q + 1]); } \
;                 asm volatile("" ::: "memory"); } while (0)
; DI void ph_rowpass(const Frame& F) {
;     ...
;             f32x4 wq0[4], wq1[4], wq2[4];
;     ...
;             RT_LD(wq0, 0); RT_LD(wq1, 1);
; #pragma unroll
;             for (int t = 0; t < 30; t += 3) { RT_LD(wq2, t + 2); RT_FMA(wq0, t); RT_LD(wq0, t + 3); RT_FMA(wq1, t + 1); RT_LD(wq1, t + 4); RT_FMA(wq2, t + 2); }
;             RT_FMA(wq0, 30); RT_FMA(wq1, 31);
	v_pk_fma_f32 v[196:197], v[28:29], v[32:33], v[198:199] op_sel_hi:[0,1,1]
	v_pk_fma_f32 v[198:199], v[28:29], v[34:35], v[200:201] op_sel_hi:[0,1,1]
	s_waitcnt lgkmcnt(10)
	v_pk_fma_f32 v[200:201], v[28:29], v[170:171], v[202:203] op_sel_hi:[0,1,1]
	v_pk_fma_f32 v[202:203], v[28:29], v[172:173], v[204:205] op_sel_hi:[0,1,1]
	s_waitcnt lgkmcnt(9)
	v_pk_fma_f32 v[204:205], v[28:29], v[174:175], v[206:207] op_sel_hi:[0,1,1]
	v_pk_fma_f32 v[206:207], v[28:29], v[176:177], v[208:209] op_sel_hi:[0,1,1]
	s_waitcnt lgkmcnt(8)
	v_pk_fma_f32 v[178:179], v[28:29], v[178:179], v[194:195] op_sel_hi:[0,1,1]
	v_pk_fma_f32 v[180:181], v[28:29], v[180:181], v[30:31] op_sel_hi:[0,1,1]
	ds_read_b128 v[28:31], v87
	ds_read_b128 v[32:35], v88
	ds_read_b128 v[170:173], v89
	ds_read_b128 v[174:177], v90
	s_waitcnt lgkmcnt(11)
	v_pk_fma_f32 v[194:195], v[26:27], v[36:37], v[196:197] op_sel_hi:[0,1,1]
	v_pk_fma_f32 v[196:197], v[26:27], v[38:39], v[198:199] op_sel_hi:[0,1,1]
	s_waitcnt lgkmcnt(10)
	v_pk_fma_f32 v[198:199], v[26:27], v[182:183], v[200:201] op_sel_hi:[0,1,1]
	v_pk_fma_f32 v[200:201], v[26:27], v[184:185], v[202:203] op_sel_hi:[0,1,1]
	s_waitcnt lgkmcnt(9)
	v_pk_fma_f32 v[202:203], v[26:27], v[186:187], v[204:205] op_sel_hi:[0,1,1]
	v_pk_fma_f32 v[204:205], v[26:27], v[188:189], v[206:207] op_sel_hi:[0,1,1]
	s_waitcnt lgkmcnt(8)
	v_pk_fma_f32 v[190:191], v[26:27], v[190:191], v[178:179] op_sel_hi:[0,1,1]
	v_pk_fma_f32 v[26:27], v[26:27], v[192:193], v[180:181] op_sel_hi:[0,1,1]
	ds_read_b128 v[36:39], v91
	ds_read_b128 v[178:181], v92
	ds_read_b128 v[182:185], v93
	ds_read_b128 v[186:189], v94
	v_mov_b32_e32 v2, v15
	s_waitcnt lgkmcnt(11)
	v_pk_fma_f32 v[192:193], v[2:3], v[154:155], v[194:195] op_sel_hi:[0,1,1]
	v_pk_fma_f32 v[194:195], v[2:3], v[156:157], v[196:197] op_sel_hi:[0,1,1]
	s_waitcnt lgkmcnt(10)
	v_pk_fma_f32 v[196:197], v[2:3], v[158:159], v[198:199] op_sel_hi:[0,1,1]
	v_pk_fma_f32 v[198:199], v[2:3], v[160:161], v[200:201] op_sel_hi:[0,1,1]
	s_waitcnt lgkmcnt(9)
	v_pk_fma_f32 v[200:201], v[2:3], v[162:163], v[202:203] op_sel_hi:[0,1,1]
	v_pk_fma_f32 v[202:203], v[2:3], v[164:165], v[204:205] op_sel_hi:[0,1,1]
	s_waitcnt lgkmcnt(8)
	v_pk_fma_f32 v[190:191], v[2:3], v[166:167], v[190:191] op_sel_hi:[0,1,1]
	v_pk_fma_f32 v[26:27], v[2:3], v[168:169], v[26:27] op_sel_hi:[0,1,1]
	ds_read_b128 v[154:157], v95
	ds_read_b128 v[158:161], v96
	ds_read_b128 v[162:165], v97
	ds_read_b128 v[166:169], v98
	s_waitcnt lgkmcnt(11)
	v_pk_fma_f32 v[192:193], v[24:25], v[28:29], v[192:193] op_sel_hi:[0,1,1]
	v_pk_fma_f32 v[194:195], v[24:25], v[30:31], v[194:195] op_sel_hi:[0,1,1]
	s_waitcnt lgkmcnt(10)
	v_pk_fma_f32 v[196:197], v[24:25], v[32:33], v[196:197] op_sel_hi:[0,1,1]
	v_pk_fma_f32 v[198:199], v[24:25], v[34:35], v[198:199] op_sel_hi:[0,1,1]
	s_waitcnt lgkmcnt(9)
	v_pk_fma_f32 v[200:201], v[24:25], v[170:171], v[200:201] op_sel_hi:[0,1,1]
	v_pk_fma_f32 v[202:203], v[24:25], v[172:173], v[202:203] op_sel_hi:[0,1,1]
	s_waitcnt lgkmcnt(8)
	v_pk_fma_f32 v[174:175], v[24:25], v[174:175], v[190:191] op_sel_hi:[0,1,1]
	v_pk_fma_f32 v[176:177], v[24:25], v[176:177], v[26:27] op_sel_hi:[0,1,1]
	ds_read_b128 v[24:27], v99
	ds_read_b128 v[28:31], v100
	ds_read_b128 v[32:35], v101
	ds_read_b128 v[170:173], v102
	s_waitcnt lgkmcnt(11)
	v_pk_fma_f32 v[190:191], v[22:23], v[36:37], v[192:193] op_sel_hi:[0,1,1]
	v_pk_fma_f32 v[192:193], v[22:23], v[38:39], v[194:195] op_sel_hi:[0,1,1]
	s_waitcnt lgkmcnt(10)
	v_pk_fma_f32 v[194:195], v[22:23], v[178:179], v[196:197] op_sel_hi:[0,1,1]
	v_pk_fma_f32 v[196:197], v[22:23], v[180:181], v[198:199] op_sel_hi:[0,1,1]
	s_waitcnt lgkmcnt(9)
	v_pk_fma_f32 v[198:199], v[22:23], v[182:183], v[200:201] op_sel_hi:[0,1,1]
	v_pk_fma_f32 v[200:201], v[22:23], v[184:185], v[202:203] op_sel_hi:[0,1,1]
	s_waitcnt lgkmcnt(8)
	v_pk_fma_f32 v[186:187], v[22:23], v[186:187], v[174:175] op_sel_hi:[0,1,1]
	v_pk_fma_f32 v[22:23], v[22:23], v[188:189], v[176:177] op_sel_hi:[0,1,1]
	ds_read_b128 v[36:39], v103
	ds_read_b128 v[174:177], v104
	ds_read_b128 v[178:181], v105
	ds_read_b128 v[182:185], v106
	s_waitcnt lgkmcnt(11)
	v_pk_fma_f32 v[188:189], v[20:21], v[154:155], v[190:191] op_sel_hi:[0,1,1]
	v_pk_fma_f32 v[190:191], v[20:21], v[156:157], v[192:193] op_sel_hi:[0,1,1]
	s_waitcnt lgkmcnt(10)
	v_pk_fma_f32 v[192:193], v[20:21], v[158:159], v[194:195] op_sel_hi:[0,1,1]
	v_pk_fma_f32 v[194:195], v[20:21], v[160:161], v[196:197] op_sel_hi:[0,1,1]
	s_waitcnt lgkmcnt(9)
	v_pk_fma_f32 v[196:197], v[20:21], v[162:163], v[198:199] op_sel_hi:[0,1,1]
	v_pk_fma_f32 v[198:199], v[20:21], v[164:165], v[200:201] op_sel_hi:[0,1,1]
	s_waitcnt lgkmcnt(8)
	v_pk_fma_f32 v[166:167], v[20:21], v[166:167], v[186:187] op_sel_hi:[0,1,1]
	v_pk_fma_f32 v[168:169], v[20:21], v[168:169], v[22:23] op_sel_hi:[0,1,1]
	ds_read_b128 v[20:23], v107
	ds_read_b128 v[154:157], v108
	ds_read_b128 v[158:161], v109
	ds_read_b128 v[162:165], v110
	v_mov_b32_e32 v2, v9
	s_waitcnt lgkmcnt(11)
	v_pk_fma_f32 v[186:187], v[2:3], v[24:25], v[188:189] op_sel_hi:[0,1,1]
	v_pk_fma_f32 v[188:189], v[2:3], v[26:27], v[190:191] op_sel_hi:[0,1,1]
	s_waitcnt lgkmcnt(10)
	v_pk_fma_f32 v[190:191], v[2:3], v[28:29], v[192:193] op_sel_hi:[0,1,1]
	v_pk_fma_f32 v[192:193], v[2:3], v[30:31], v[194:195] op_sel_hi:[0,1,1]
	s_waitcnt lgkmcnt(9)
	v_pk_fma_f32 v[194:195], v[2:3], v[32:33], v[196:197] op_sel_hi:[0,1,1]
	v_pk_fma_f32 v[196:197], v[2:3], v[34:35], v[198:199] op_sel_hi:[0,1,1]
	s_waitcnt lgkmcnt(8)
	v_pk_fma_f32 v[170:171], v[2:3], v[170:171], v[166:167] op_sel_hi:[0,1,1]
	v_pk_fma_f32 v[172:173], v[2:3], v[172:173], v[168:169] op_sel_hi:[0,1,1]
	ds_read_b128 v[24:27], v111
	ds_read_b128 v[28:31], v112
	ds_read_b128 v[32:35], v113
	ds_read_b128 v[166:169], v114
	s_waitcnt lgkmcnt(11)
; #define RT_LD(W, t_) do { _Pragma("unroll") for (int q = 0; q < 4; ++q) W[q] = wl[((((t_)) * 4 + q) << 6) + F.lane]; } while (0)
; #define RT_FMA(W, t_) do { const float hv_ = v[(t_) >> 2][(t_) & 3]; const f32x2 hh = {hv_, hv_}; _Pragma("unroll") for (int q = 0; q < 4; ++q) { \
;                 lgp[2 * q] = __builtin_elementwise_fma(hh, (f32x2){W[q][0], W[q][1]}, lgp[2 * q]); lgp[2 * q + 1] = __builtin_elementwise_fma(hh, (f32x2){W[q][2], W[q][3]}, lgp[2 * q + 1]); } \
;                 asm volatile("" ::: "memory"); } while (0)
; DI void ph_rowpass(const Frame& F) {
;     ...
;             f32x4 wq0[4], wq1[4], wq2[4];
;     ...
;             RT_LD(wq0, 0); RT_LD(wq1, 1);
; #pragma unroll
;             for (int t = 0; t < 30; t += 3) { RT_LD(wq2, t + 2); RT_FMA(wq0, t); RT_LD(wq0, t + 3); RT_FMA(wq1, t + 1); RT_LD(wq1, t + 4); RT_FMA(wq2, t + 2); }
;             RT_FMA(wq0, 30); RT_FMA(wq1, 31);
	v_pk_fma_f32 v[186:187], v[18:19], v[36:37], v[186:187] op_sel_hi:[0,1,1]
	v_pk_fma_f32 v[188:189], v[18:19], v[38:39], v[188:189] op_sel_hi:[0,1,1]
	s_waitcnt lgkmcnt(10)
	v_pk_fma_f32 v[190:191], v[18:19], v[174:175], v[190:191] op_sel_hi:[0,1,1]
	v_pk_fma_f32 v[192:193], v[18:19], v[176:177], v[192:193] op_sel_hi:[0,1,1]
	s_waitcnt lgkmcnt(9)
	v_pk_fma_f32 v[194:195], v[18:19], v[178:179], v[194:195] op_sel_hi:[0,1,1]
	v_pk_fma_f32 v[196:197], v[18:19], v[180:181], v[196:197] op_sel_hi:[0,1,1]
	s_waitcnt lgkmcnt(8)
	v_pk_fma_f32 v[182:183], v[18:19], v[182:183], v[170:171] op_sel_hi:[0,1,1]
	v_pk_fma_f32 v[18:19], v[18:19], v[184:185], v[172:173] op_sel_hi:[0,1,1]
	ds_read_b128 v[36:39], v115
	ds_read_b128 v[170:173], v116
	ds_read_b128 v[174:177], v117
	ds_read_b128 v[178:181], v118
	s_waitcnt lgkmcnt(11)
	v_pk_fma_f32 v[184:185], v[16:17], v[20:21], v[186:187] op_sel_hi:[0,1,1]
	v_pk_fma_f32 v[186:187], v[16:17], v[22:23], v[188:189] op_sel_hi:[0,1,1]
	s_waitcnt lgkmcnt(10)
	v_pk_fma_f32 v[188:189], v[16:17], v[154:155], v[190:191] op_sel_hi:[0,1,1]
	v_pk_fma_f32 v[190:191], v[16:17], v[156:157], v[192:193] op_sel_hi:[0,1,1]
	s_waitcnt lgkmcnt(9)
	v_pk_fma_f32 v[192:193], v[16:17], v[158:159], v[194:195] op_sel_hi:[0,1,1]
	v_pk_fma_f32 v[194:195], v[16:17], v[160:161], v[196:197] op_sel_hi:[0,1,1]
	s_waitcnt lgkmcnt(8)
	v_pk_fma_f32 v[162:163], v[16:17], v[162:163], v[182:183] op_sel_hi:[0,1,1]
	v_pk_fma_f32 v[164:165], v[16:17], v[164:165], v[18:19] op_sel_hi:[0,1,1]
	ds_read_b128 v[16:19], v119
	ds_read_b128 v[20:23], v120
	ds_read_b128 v[154:157], v121
	ds_read_b128 v[158:161], v122
	s_waitcnt lgkmcnt(11)
	v_pk_fma_f32 v[182:183], v[14:15], v[24:25], v[184:185] op_sel_hi:[0,1,1]
	v_pk_fma_f32 v[184:185], v[14:15], v[26:27], v[186:187] op_sel_hi:[0,1,1]
	s_waitcnt lgkmcnt(10)
	v_pk_fma_f32 v[186:187], v[14:15], v[28:29], v[188:189] op_sel_hi:[0,1,1]
	v_pk_fma_f32 v[188:189], v[14:15], v[30:31], v[190:191] op_sel_hi:[0,1,1]
	s_waitcnt lgkmcnt(9)
	v_pk_fma_f32 v[190:191], v[14:15], v[32:33], v[192:193] op_sel_hi:[0,1,1]
	v_pk_fma_f32 v[192:193], v[14:15], v[34:35], v[194:195] op_sel_hi:[0,1,1]
	s_waitcnt lgkmcnt(8)
	v_pk_fma_f32 v[166:167], v[14:15], v[166:167], v[162:163] op_sel_hi:[0,1,1]
	v_pk_fma_f32 v[14:15], v[14:15], v[168:169], v[164:165] op_sel_hi:[0,1,1]
	ds_read_b128 v[24:27], v123
	ds_read_b128 v[28:31], v124
	ds_read_b128 v[32:35], v125
	ds_read_b128 v[162:165], v126
	v_mov_b32_e32 v2, v7
	s_waitcnt lgkmcnt(11)
	v_pk_fma_f32 v[182:183], v[2:3], v[36:37], v[182:183] op_sel_hi:[0,1,1]
	v_pk_fma_f32 v[184:185], v[2:3], v[38:39], v[184:185] op_sel_hi:[0,1,1]
	s_waitcnt lgkmcnt(10)
	v_pk_fma_f32 v[186:187], v[2:3], v[170:171], v[186:187] op_sel_hi:[0,1,1]
	v_pk_fma_f32 v[188:189], v[2:3], v[172:173], v[188:189] op_sel_hi:[0,1,1]
	s_waitcnt lgkmcnt(9)
	v_pk_fma_f32 v[190:191], v[2:3], v[174:175], v[190:191] op_sel_hi:[0,1,1]
	v_pk_fma_f32 v[192:193], v[2:3], v[176:177], v[192:193] op_sel_hi:[0,1,1]
	s_waitcnt lgkmcnt(8)
	v_pk_fma_f32 v[178:179], v[2:3], v[178:179], v[166:167] op_sel_hi:[0,1,1]
	v_pk_fma_f32 v[14:15], v[2:3], v[180:181], v[14:15] op_sel_hi:[0,1,1]
	ds_read_b128 v[36:39], v127
	ds_read_b128 v[166:169], v128
	ds_read_b128 v[170:173], v129
	ds_read_b128 v[174:177], v130
	s_waitcnt lgkmcnt(11)
	v_pk_fma_f32 v[180:181], v[12:13], v[16:17], v[182:183] op_sel_hi:[0,1,1]
	v_pk_fma_f32 v[182:183], v[12:13], v[18:19], v[184:185] op_sel_hi:[0,1,1]
	s_waitcnt lgkmcnt(10)
	v_pk_fma_f32 v[184:185], v[12:13], v[20:21], v[186:187] op_sel_hi:[0,1,1]
	v_pk_fma_f32 v[186:187], v[12:13], v[22:23], v[188:189] op_sel_hi:[0,1,1]
	s_waitcnt lgkmcnt(9)
	v_pk_fma_f32 v[188:189], v[12:13], v[154:155], v[190:191] op_sel_hi:[0,1,1]
	v_pk_fma_f32 v[190:191], v[12:13], v[156:157], v[192:193] op_sel_hi:[0,1,1]
	s_waitcnt lgkmcnt(8)
	v_pk_fma_f32 v[158:159], v[12:13], v[158:159], v[178:179] op_sel_hi:[0,1,1]
	v_pk_fma_f32 v[160:161], v[12:13], v[160:161], v[14:15] op_sel_hi:[0,1,1]
	ds_read_b128 v[12:15], v131
	ds_read_b128 v[16:19], v132
	ds_read_b128 v[20:23], v133
	ds_read_b128 v[154:157], v134
	s_waitcnt lgkmcnt(11)
	v_pk_fma_f32 v[178:179], v[10:11], v[24:25], v[180:181] op_sel_hi:[0,1,1]
	v_pk_fma_f32 v[180:181], v[10:11], v[26:27], v[182:183] op_sel_hi:[0,1,1]
	s_waitcnt lgkmcnt(10)
	v_pk_fma_f32 v[182:183], v[10:11], v[28:29], v[184:185] op_sel_hi:[0,1,1]
	v_pk_fma_f32 v[184:185], v[10:11], v[30:31], v[186:187] op_sel_hi:[0,1,1]
	s_waitcnt lgkmcnt(9)
	v_pk_fma_f32 v[186:187], v[10:11], v[32:33], v[188:189] op_sel_hi:[0,1,1]
	v_pk_fma_f32 v[188:189], v[10:11], v[34:35], v[190:191] op_sel_hi:[0,1,1]
	s_waitcnt lgkmcnt(8)
	v_pk_fma_f32 v[162:163], v[10:11], v[162:163], v[158:159] op_sel_hi:[0,1,1]
	v_pk_fma_f32 v[10:11], v[10:11], v[164:165], v[160:161] op_sel_hi:[0,1,1]
	ds_read_b128 v[24:27], v135
	ds_read_b128 v[28:31], v136
	ds_read_b128 v[32:35], v137
	ds_read_b128 v[158:161], v138
	s_waitcnt lgkmcnt(11)
	v_pk_fma_f32 v[178:179], v[8:9], v[36:37], v[178:179] op_sel_hi:[0,1,1]
	v_pk_fma_f32 v[180:181], v[8:9], v[38:39], v[180:181] op_sel_hi:[0,1,1]
	s_waitcnt lgkmcnt(10)
	v_pk_fma_f32 v[182:183], v[8:9], v[166:167], v[182:183] op_sel_hi:[0,1,1]
	v_pk_fma_f32 v[184:185], v[8:9], v[168:169], v[184:185] op_sel_hi:[0,1,1]
	s_waitcnt lgkmcnt(9)
	v_pk_fma_f32 v[170:171], v[8:9], v[170:171], v[186:187] op_sel_hi:[0,1,1]
	v_pk_fma_f32 v[172:173], v[8:9], v[172:173], v[188:189] op_sel_hi:[0,1,1]
	s_waitcnt lgkmcnt(8)
	v_pk_fma_f32 v[174:175], v[8:9], v[174:175], v[162:163] op_sel_hi:[0,1,1]
	v_pk_fma_f32 v[176:177], v[8:9], v[176:177], v[10:11] op_sel_hi:[0,1,1]
	ds_read_b128 v[8:11], v139
	ds_read_b128 v[36:39], v140
	ds_read_b128 v[162:165], v141
	ds_read_b128 v[166:169], v142
	v_mov_b32_e32 v2, v5
	s_waitcnt lgkmcnt(11)
; DI float swz16_f(float v) { return __builtin_bit_cast(float, __builtin_amdgcn_ds_swizzle(__builtin_bit_cast(int, v), 0x401F)); }
; #define RT_LD(W, t_) do { _Pragma("unroll") for (int q = 0; q < 4; ++q) W[q] = wl[((((t_)) * 4 + q) << 6) + F.lane]; } while (0)
; DI float expert_totals16(const f32x2 (&p)[8], int lane) {
;     float y[8];
; #pragma unroll
;     for (int i = 0; i < 8; ++i) { const float a = p[i >> 1][i & 1], b = p[(i + 8) >> 1][i & 1];
;         auto r = __builtin_amdgcn_permlane32_swap(__float_as_uint(a), __float_as_uint(b), false, false); y[i] = __uint_as_float(r[0]) + __uint_as_float(r[1]); }
;     const bool b4 = (lane & 16) != 0, b3 = (lane & 8) != 0, b2 = (lane & 4) != 0;
;     float z[4];
; #pragma unroll
;     for (int i = 0; i < 4; ++i) { const float send = b4 ? y[i] : y[i + 4], keep = b4 ? y[i + 4] : y[i]; z[i] = keep + swz16_f(send); }
;     float w[2];
; #pragma unroll
;     for (int i = 0; i < 2; ++i) { const float send = b3 ? z[i] : z[i + 2], keep = b3 ? z[i + 2] : z[i]; w[i] = keep + dpp_f(send, 0x128); }
;     float v; { const float send = b2 ? w[0] : w[1], keep = b2 ? w[1] : w[0]; v = keep + dpp_f(send, 0x141); }
;     v += dpp_f(v, 0xB1); v += dpp_f(v, 0x4E);
;     return v;
; }
; DI float experts_max(float v) { v = fmaxf(v, dpp_f(v, 0x141)); v = fmaxf(v, dpp_f(v, 0x140)); v = fmaxf(v, swz16_f(v));
;     auto r = __builtin_amdgcn_permlane32_swap(__float_as_uint(v), __float_as_uint(v), false, false); return fmaxf(__uint_as_float(r[0]), __uint_as_float(r[1])); }
; DI float experts_sum(float v) { v += dpp_f(v, 0x141); v += dpp_f(v, 0x140); v += swz16_f(v);
;     auto r = __builtin_amdgcn_permlane32_swap(__float_as_uint(v), __float_as_uint(v), false, false); return __uint_as_float(r[0]) + __uint_as_float(r[1]); }
; DI void ph_rowpass(const Frame& F) {
;     ...
;             for (int t = 0; t < 30; t += 3) { RT_LD(wq2, t + 2); RT_FMA(wq0, t); RT_LD(wq0, t + 3); RT_FMA(wq1, t + 1); RT_LD(wq1, t + 4); RT_FMA(wq2, t + 2); }
;             RT_FMA(wq0, 30); RT_FMA(wq1, 31);
;     ...
;         }
;         {
;             const float tot = expert_totals16(lgp, F.lane);
;             const float pe = __expf(tot - experts_max(tot));
;             const float prob = pe * (1.f / experts_sum(pe));
;             if ((F.lane & 3) == 0) AFF[((size_t)b * NE + (F.lane >> 2)) * S + s] = prob;
;         }
	v_pk_fma_f32 v[178:179], v[2:3], v[12:13], v[178:179] op_sel_hi:[0,1,1]
	v_pk_fma_f32 v[180:181], v[2:3], v[14:15], v[180:181] op_sel_hi:[0,1,1]
	s_waitcnt lgkmcnt(10)
	v_pk_fma_f32 v[182:183], v[2:3], v[16:17], v[182:183] op_sel_hi:[0,1,1]
	v_pk_fma_f32 v[184:185], v[2:3], v[18:19], v[184:185] op_sel_hi:[0,1,1]
	s_waitcnt lgkmcnt(9)
	v_pk_fma_f32 v[170:171], v[2:3], v[20:21], v[170:171] op_sel_hi:[0,1,1]
	v_pk_fma_f32 v[172:173], v[2:3], v[22:23], v[172:173] op_sel_hi:[0,1,1]
	s_waitcnt lgkmcnt(8)
	v_pk_fma_f32 v[174:175], v[2:3], v[154:155], v[174:175] op_sel_hi:[0,1,1]
	v_pk_fma_f32 v[176:177], v[2:3], v[156:157], v[176:177] op_sel_hi:[0,1,1]
	ds_read_b128 v[12:15], v143
	ds_read_b128 v[16:19], v144
	ds_read_b128 v[20:23], v145
	ds_read_b128 v[154:157], v146
	s_waitcnt lgkmcnt(11)
	v_pk_fma_f32 v[178:179], v[6:7], v[24:25], v[178:179] op_sel_hi:[0,1,1]
	v_pk_fma_f32 v[180:181], v[6:7], v[26:27], v[180:181] op_sel_hi:[0,1,1]
	s_waitcnt lgkmcnt(10)
	v_pk_fma_f32 v[182:183], v[6:7], v[28:29], v[182:183] op_sel_hi:[0,1,1]
	v_pk_fma_f32 v[184:185], v[6:7], v[30:31], v[184:185] op_sel_hi:[0,1,1]
	s_waitcnt lgkmcnt(9)
	v_pk_fma_f32 v[170:171], v[6:7], v[32:33], v[170:171] op_sel_hi:[0,1,1]
	v_pk_fma_f32 v[172:173], v[6:7], v[34:35], v[172:173] op_sel_hi:[0,1,1]
	s_waitcnt lgkmcnt(8)
	v_pk_fma_f32 v[174:175], v[6:7], v[158:159], v[174:175] op_sel_hi:[0,1,1]
	v_pk_fma_f32 v[6:7], v[6:7], v[160:161], v[176:177] op_sel_hi:[0,1,1]
	ds_read_b128 v[24:27], v147
	ds_read_b128 v[28:31], v148
	ds_read_b128 v[32:35], v149
	ds_read_b128 v[158:161], v150
	s_waitcnt lgkmcnt(11)
	v_pk_fma_f32 v[8:9], v[4:5], v[8:9], v[178:179] op_sel_hi:[0,1,1]
	v_pk_fma_f32 v[10:11], v[4:5], v[10:11], v[180:181] op_sel_hi:[0,1,1]
	s_waitcnt lgkmcnt(10)
	v_pk_fma_f32 v[36:37], v[4:5], v[36:37], v[182:183] op_sel_hi:[0,1,1]
	v_pk_fma_f32 v[38:39], v[4:5], v[38:39], v[184:185] op_sel_hi:[0,1,1]
	s_waitcnt lgkmcnt(9)
	v_pk_fma_f32 v[162:163], v[4:5], v[162:163], v[170:171] op_sel_hi:[0,1,1]
	v_pk_fma_f32 v[164:165], v[4:5], v[164:165], v[172:173] op_sel_hi:[0,1,1]
	s_waitcnt lgkmcnt(8)
	v_pk_fma_f32 v[166:167], v[4:5], v[166:167], v[174:175] op_sel_hi:[0,1,1]
	v_pk_fma_f32 v[4:5], v[4:5], v[168:169], v[6:7] op_sel_hi:[0,1,1]
	s_waitcnt lgkmcnt(7)
	v_pk_fma_f32 v[6:7], v[0:1], v[12:13], v[8:9] op_sel_hi:[0,1,1]
	v_pk_fma_f32 v[8:9], v[0:1], v[14:15], v[10:11] op_sel_hi:[0,1,1]
	s_waitcnt lgkmcnt(6)
	v_pk_fma_f32 v[10:11], v[0:1], v[16:17], v[36:37] op_sel_hi:[0,1,1]
	v_pk_fma_f32 v[12:13], v[0:1], v[18:19], v[38:39] op_sel_hi:[0,1,1]
	s_waitcnt lgkmcnt(5)
	v_pk_fma_f32 v[14:15], v[0:1], v[20:21], v[162:163] op_sel_hi:[0,1,1]
	v_pk_fma_f32 v[16:17], v[0:1], v[22:23], v[164:165] op_sel_hi:[0,1,1]
	s_waitcnt lgkmcnt(4)
	v_pk_fma_f32 v[18:19], v[0:1], v[154:155], v[166:167] op_sel_hi:[0,1,1]
	v_mov_b32_e32 v2, v3
	v_pk_fma_f32 v[0:1], v[0:1], v[156:157], v[4:5] op_sel_hi:[0,1,1]
	s_waitcnt lgkmcnt(3)
	v_pk_fma_f32 v[4:5], v[2:3], v[24:25], v[6:7] op_sel_hi:[0,1,1]
	v_pk_fma_f32 v[6:7], v[2:3], v[26:27], v[8:9] op_sel_hi:[0,1,1]
	s_waitcnt lgkmcnt(2)
	v_pk_fma_f32 v[8:9], v[2:3], v[28:29], v[10:11] op_sel_hi:[0,1,1]
	v_pk_fma_f32 v[10:11], v[2:3], v[30:31], v[12:13] op_sel_hi:[0,1,1]
	s_waitcnt lgkmcnt(1)
	v_pk_fma_f32 v[12:13], v[2:3], v[32:33], v[14:15] op_sel_hi:[0,1,1]
	v_pk_fma_f32 v[14:15], v[2:3], v[34:35], v[16:17] op_sel_hi:[0,1,1]
	s_waitcnt lgkmcnt(0)
	v_pk_fma_f32 v[16:17], v[2:3], v[158:159], v[18:19] op_sel_hi:[0,1,1]
	v_permlane32_swap_b32_e32 v4, v12
	v_permlane32_swap_b32_e32 v6, v14
	v_permlane32_swap_b32_e32 v8, v16
	v_pk_fma_f32 v[0:1], v[2:3], v[160:161], v[0:1] op_sel_hi:[0,1,1]
	v_add_f32_e32 v2, v4, v12
	v_add_f32_e32 v4, v6, v14
	v_add_f32_e32 v6, v8, v16
	v_cndmask_b32_e64 v8, v2, v6, s[2:3]
	ds_swizzle_b32 v8, v8 offset:swizzle(SWAP,16)
	v_permlane32_swap_b32_e32 v5, v13
	v_permlane32_swap_b32_e32 v7, v15
	v_permlane32_swap_b32_e32 v9, v17
	v_permlane32_swap_b32_e32 v10, v0
	v_permlane32_swap_b32_e32 v11, v1
	v_add_f32_e32 v3, v5, v13
	v_add_f32_e32 v5, v7, v15
	v_add_f32_e32 v7, v9, v17
	v_add_f32_e32 v0, v10, v0
	v_add_f32_e32 v1, v11, v1
	v_cndmask_b32_e64 v2, v6, v2, s[2:3]
	s_waitcnt lgkmcnt(0)
	v_add_f32_e32 v2, v2, v8
	v_cndmask_b32_e64 v6, v3, v7, s[2:3]
	v_cndmask_b32_e64 v3, v7, v3, s[2:3]
	v_cndmask_b32_e64 v7, v4, v0, s[2:3]
	v_cndmask_b32_e64 v8, v5, v1, s[2:3]
	ds_swizzle_b32 v6, v6 offset:swizzle(SWAP,16)
	ds_swizzle_b32 v7, v7 offset:swizzle(SWAP,16)
	ds_swizzle_b32 v8, v8 offset:swizzle(SWAP,16)
	v_cndmask_b32_e64 v0, v0, v4, s[2:3]
	v_cndmask_b32_e64 v1, v1, v5, s[2:3]
	s_waitcnt lgkmcnt(2)
	v_add_f32_e32 v3, v3, v6
	s_waitcnt lgkmcnt(1)
	v_add_f32_e32 v0, v0, v7
	s_waitcnt lgkmcnt(0)
	v_add_f32_e32 v1, v1, v8
	v_cndmask_b32_e64 v4, v2, v0, s[4:5]
	v_cndmask_b32_e64 v0, v0, v2, s[4:5]
	v_cndmask_b32_e64 v2, v3, v1, s[4:5]
	v_cndmask_b32_e64 v1, v1, v3, s[4:5]
	v_add_f32_dpp v0, v4, v0 row_ror:8 row_mask:0xf bank_mask:0xf bound_ctrl:1
	s_nop 0
	v_add_f32_dpp v1, v2, v1 row_ror:8 row_mask:0xf bank_mask:0xf bound_ctrl:1
	v_cndmask_b32_e64 v2, v0, v1, s[6:7]
	v_cndmask_b32_e64 v0, v1, v0, s[6:7]
	s_nop 1
	v_add_f32_dpp v0, v2, v0 row_half_mirror row_mask:0xf bank_mask:0xf bound_ctrl:1
	s_nop 1
	v_add_f32_dpp v0, v0, v0 quad_perm:[1,0,3,2] row_mask:0xf bank_mask:0xf bound_ctrl:1
	s_nop 1
	v_add_f32_dpp v0, v0, v0 quad_perm:[2,3,0,1] row_mask:0xf bank_mask:0xf bound_ctrl:1
	s_nop 1
	v_mov_b32_dpp v1, v0 row_half_mirror row_mask:0xf bank_mask:0xf bound_ctrl:1
	v_max_f32_e32 v1, v1, v1
	v_max_f32_e32 v1, v0, v1
	s_nop 1
	v_mov_b32_dpp v2, v1 row_mirror row_mask:0xf bank_mask:0xf bound_ctrl:1
	v_max_f32_e32 v2, v2, v2
	v_max_f32_e32 v1, v1, v2
	ds_swizzle_b32 v2, v1 offset:swizzle(SWAP,16)
	s_waitcnt lgkmcnt(0)
	v_max_f32_e32 v2, v2, v2
	v_max_f32_e32 v1, v1, v2
	v_mov_b32_e32 v2, v1
	s_nop 1
	v_permlane32_swap_b32_e32 v1, v2
	v_max_f32_e32 v2, v2, v2
	v_max_f32_e32 v1, v1, v1
	v_max_f32_e32 v1, v1, v2
	v_sub_f32_e32 v0, v0, v1
	v_mul_f32_e32 v0, 0x3fb8aa3b, v0
	v_exp_f32_e32 v0, v0
	s_nop 1
	v_add_f32_dpp v1, v0, v0 row_half_mirror row_mask:0xf bank_mask:0xf bound_ctrl:1
	s_nop 1
	v_add_f32_dpp v1, v1, v1 row_mirror row_mask:0xf bank_mask:0xf bound_ctrl:1
	ds_swizzle_b32 v2, v1 offset:swizzle(SWAP,16)
	s_waitcnt lgkmcnt(0)
	v_add_f32_e32 v1, v1, v2
	v_mov_b32_e32 v2, v1
	s_nop 1
	v_permlane32_swap_b32_e32 v1, v2
	s_and_saveexec_b64 s[22:23], s[8:9]
	s_cbranch_execz .LBB4_1122
	v_add_f32_e32 v1, v1, v2
	v_div_scale_f32 v2, s[42:43], v1, v1, 1.0
	v_rcp_f32_e32 v3, v2
	s_ashr_i32 s42, s18, 12
	s_ashr_i32 s43, s42, 31
	s_lshl_b64 s[42:43], s[42:43], 18
	v_fma_f32 v4, -v2, v3, 1.0
	v_fmac_f32_e32 v3, v4, v3
	v_div_scale_f32 v4, vcc, 1.0, v1, 1.0
	v_mul_f32_e32 v5, v4, v3
	v_fma_f32 v6, -v2, v5, v4
	v_fmac_f32_e32 v5, v6, v3
	v_fma_f32 v2, -v2, v5, v4
	v_div_fmas_f32 v2, v2, v3, v5
	s_add_u32 s42, s46, s42
	v_div_fixup_f32 v1, v2, v1, 1.0
	s_addc_u32 s43, s47, s43
	v_mul_f32_e32 v2, v0, v1
	v_lshl_add_u64 v[0:1], s[42:43], 0, v[56:57]
	global_store_dword v[0:1], v2, off
	s_branch .LBB4_1122

; #define LAS __attribute__((address_space(3)))
; #define REFRESH() do { F.tid = tid_fresh(F.wave); F.lane = F.tid & 63; } while (0)
; __global__ void __launch_bounds__(NTHR, 2) mega(Args a) {
;     extern __shared__ __attribute__((aligned(16))) unsigned char lds[];
;     Frame F;
;     F.lds = lds; F.ldsl = (LAS unsigned char*)lds; F.ws = a.ws; F.in = a.in; F.out = a.out;
;     F.wg = blockIdx.x; F.nwg = gridDim.x;
;     F.wave = __builtin_amdgcn_readfirstlane(threadIdx.x >> 6);
;     ...
;     REFRESH();
;     for (int u = F.tid; u < (LDS_BYTES - LDSCTL_OFF) / 4; u += NTHR) ((unsigned*)(lds + LDSCTL_OFF))[u] = 0u;
;     __syncthreads();
;     const int lo = a.ph_lo, hi = a.ph_hi;
;     XcdBarrier bar; bar.bar = (unsigned*)(a.ws + WS_CTL) + CW_BAR; bar.x = 0; bar.st = nullptr; bar.wave = F.wave;
;     if (hi - lo > 1) bar = xcd_barrier_post((unsigned*)(a.ws + WS_CTL) + CW_BAR, (volatile LAS unsigned*)(lds + MISC_OFF + 32), F.wave);
	.amdhsa_kernel _Z4mega4Args
		.amdhsa_group_segment_fixed_size 0
		.amdhsa_private_segment_fixed_size 0
		.amdhsa_kernarg_size 456
		.amdhsa_user_sgpr_count 2
		.amdhsa_user_sgpr_dispatch_ptr 0
		.amdhsa_user_sgpr_queue_ptr 0
		.amdhsa_user_sgpr_kernarg_segment_ptr 1
		.amdhsa_user_sgpr_dispatch_id 0
		.amdhsa_user_sgpr_kernarg_preload_length 0
		.amdhsa_user_sgpr_kernarg_preload_offset 0
		.amdhsa_user_sgpr_private_segment_size 0
		.amdhsa_uses_dynamic_stack 0
		.amdhsa_enable_private_segment 0
		.amdhsa_system_sgpr_workgroup_id_x 1
		.amdhsa_system_sgpr_workgroup_id_y 0
		.amdhsa_system_sgpr_workgroup_id_z 0
		.amdhsa_system_sgpr_workgroup_info 0
		.amdhsa_system_vgpr_workitem_id 0
		.amdhsa_next_free_vgpr 256
		.amdhsa_next_free_sgpr 96
		.amdhsa_accum_offset 256
		.amdhsa_reserve_vcc 1
		.amdhsa_float_round_mode_32 0
		.amdhsa_float_round_mode_16_64 0
		.amdhsa_float_denorm_mode_32 3
		.amdhsa_float_denorm_mode_16_64 3
		.amdhsa_dx10_clamp 1
		.amdhsa_ieee_mode 1
		.amdhsa_fp16_overflow 0
		.amdhsa_tg_split 0
		.amdhsa_exception_fp_ieee_invalid_op 0
		.amdhsa_exception_fp_denorm_src 0
		.amdhsa_exception_fp_ieee_div_zero 0
		.amdhsa_exception_fp_ieee_overflow 0
		.amdhsa_exception_fp_ieee_underflow 0
		.amdhsa_exception_fp_ieee_inexact 0
		.amdhsa_exception_int_div_zero 0
	.end_amdhsa_kernel

; __global__ void __launch_bounds__(256) k_attn_naive(const bf16_t* __restrict__ QD, const bf16_t* __restrict__ KD, const bf16_t* __restrict__ VD, float* __restrict__ On) {
;     __shared__ __attribute__((aligned(16))) bf16_t Ks[32][64];
;     __shared__ __attribute__((aligned(16))) bf16_t Vs[32][128];
;     const int t = threadIdx.x, bid = blockIdx.x, qb = bid & 15, bhm = bid >> 4, bh = bhm >> 1;
;     const int s = qb * 256 + t;
;     float q[64], o[128];
;     {
;         const u32x4* qp = (const u32x4*)(QD + ((size_t)bhm * S + s) * 64);
; #pragma unroll
;         for (int c = 0; c < 8; ++c) { const u32x4 w = qp[c]; q[8 * c] = bflo(w.x); q[8 * c + 1] = bfhi(w.x); q[8 * c + 2] = bflo(w.y); q[8 * c + 3] = bfhi(w.y); q[8 * c + 4] = bflo(w.z); q[8 * c + 5] = bfhi(w.z); q[8 * c + 6] = bflo(w.w); q[8 * c + 7] = bfhi(w.w); }
;     }
; #pragma unroll
;     for (int e = 0; e < 128; ++e) o[e] = 0.f;
;     float mx = -1e30f, l = 0.f;
;     for (int m0 = 0; m0 < S; m0 += 32) {
;         __syncthreads();
;         *(u32x4*)&Ks[t >> 3][(t & 7) * 8] = *(const u32x4*)(KD + ((size_t)bhm * S + m0 + (t >> 3)) * 64 + (t & 7) * 8);
; #pragma unroll
;         for (int i = 0; i < 2; ++i) { const int idx = t + 256 * i, row = idx >> 4, ch = idx & 15; *(u32x4*)&Vs[row][ch * 8] = *(const u32x4*)(VD + ((size_t)bh * S + m0 + row) * 128 + ch * 8); }
;         __syncthreads();
;         for (int mm = 0; mm < 32; ++mm) {
;             float sc = 0.f;
; #pragma unroll
;             for (int c = 0; c < 8; ++c) { const u32x4 w = *(const u32x4*)&Ks[mm][c * 8];
;                 sc += q[8 * c] * bflo(w.x) + q[8 * c + 1] * bfhi(w.x) + q[8 * c + 2] * bflo(w.y) + q[8 * c + 3] * bfhi(w.y) + q[8 * c + 4] * bflo(w.z) + q[8 * c + 5] * bfhi(w.z) + q[8 * c + 6] * bflo(w.w) + q[8 * c + 7] * bfhi(w.w); }
;             if (sc > mx) { const float f = exp2f(mx - sc); l *= f;
; #pragma unroll
;                 for (int e = 0; e < 128; ++e) o[e] *= f;
;                 mx = sc; }
;             const float p = exp2f(sc - mx); l += p;
; #pragma unroll
;             for (int c = 0; c < 16; ++c) { const u32x4 w = *(const u32x4*)&Vs[mm][c * 8];
;                 o[8 * c] += p * bflo(w.x); o[8 * c + 1] += p * bfhi(w.x); o[8 * c + 2] += p * bflo(w.y); o[8 * c + 3] += p * bfhi(w.y); o[8 * c + 4] += p * bflo(w.z); o[8 * c + 5] += p * bfhi(w.z); o[8 * c + 6] += p * bflo(w.w); o[8 * c + 7] += p * bfhi(w.w); }
amdhsa.kernels:
  - .agpr_count:     0
    .args:
      - .actual_access:  read_only
        .address_space:  global
        .offset:         0
        .size:           8
        .value_kind:     global_buffer
      - .actual_access:  read_only
        .address_space:  global
        .offset:         8
        .size:           8
        .value_kind:     global_buffer
      - .actual_access:  read_only
        .address_space:  global
        .offset:         16
        .size:           8
        .value_kind:     global_buffer
      - .actual_access:  write_only
        .address_space:  global
        .offset:         24
        .size:           8
        .value_kind:     global_buffer
    .group_segment_fixed_size: 12288
    .kernarg_segment_align: 8
    .kernarg_segment_size: 32
    .language:       OpenCL C
    .language_version:
      - 2
      - 0
    .max_flat_workgroup_size: 256
    .name:           _Z12k_attn_naivePKtS0_S0_Pf
    .private_segment_fixed_size: 0
    .sgpr_count:     18
    .sgpr_spill_count: 0
    .symbol:         _Z12k_attn_naivePKtS0_S0_Pf.kd
    .uniform_work_group_size: 1
    .uses_dynamic_stack: false
    .vgpr_count:     232
    .vgpr_spill_count: 0
    .wavefront_size: 64
  - .agpr_count:     0
    .args:
      - .actual_access:  read_only
        .address_space:  global
        .offset:         0
        .size:           8
        .value_kind:     global_buffer
      - .address_space:  global
        .offset:         8
        .size:           8
        .value_kind:     global_buffer
      - .address_space:  global
        .offset:         16
        .size:           8
        .value_kind:     global_buffer
      - .address_space:  global
        .offset:         24
        .size:           8
        .value_kind:     global_buffer
      - .address_space:  global
        .offset:         32
        .size:           8
        .value_kind:     global_buffer
      - .actual_access:  read_only
        .address_space:  global
        .offset:         40
        .size:           8
        .value_kind:     global_buffer
      - .actual_access:  write_only
        .address_space:  global
        .offset:         48
        .size:           8
        .value_kind:     global_buffer
    .group_segment_fixed_size: 0
    .kernarg_segment_align: 8
    .kernarg_segment_size: 56
    .language:       OpenCL C
    .language_version:
      - 2
      - 0
    .max_flat_workgroup_size: 256
    .name:           _Z14k_attn_combinePKfS0_S0_S0_S0_S0_Pt
    .private_segment_fixed_size: 0
    .sgpr_count:     18
    .sgpr_spill_count: 0
    .symbol:         _Z14k_attn_combinePKfS0_S0_S0_S0_S0_Pt.kd
    .uniform_work_group_size: 1
    .uses_dynamic_stack: false
    .vgpr_count:     19
    .vgpr_spill_count: 0
    .wavefront_size: 64
  - .agpr_count:     0
    .args:
      - .actual_access:  read_only
        .address_space:  global
        .offset:         0
        .size:           8
        .value_kind:     global_buffer
      - .actual_access:  read_only
        .address_space:  global
        .offset:         8
        .size:           8
        .value_kind:     global_buffer
      - .actual_access:  read_only
        .address_space:  global
        .offset:         16
        .size:           8
        .value_kind:     global_buffer
      - .actual_access:  read_only
        .address_space:  global
        .offset:         24
        .size:           8
        .value_kind:     global_buffer
      - .actual_access:  write_only
        .address_space:  global
        .offset:         32
        .size:           8
        .value_kind:     global_buffer
    .group_segment_fixed_size: 12288
    .kernarg_segment_align: 8
    .kernarg_segment_size: 40
    .language:       OpenCL C
    .language_version:
      - 2
      - 0
    .max_flat_workgroup_size: 256
    .name:           _Z11k_ret_naivePKtS0_S0_PKfPf
    .private_segment_fixed_size: 0
    .sgpr_count:     22
    .sgpr_spill_count: 0
    .symbol:         _Z11k_ret_naivePKtS0_S0_PKfPf.kd
    .uniform_work_group_size: 1
    .uses_dynamic_stack: false
    .vgpr_count:     234
    .vgpr_spill_count: 0
    .wavefront_size: 64
; DI float bflo(unsigned w) { return __uint_as_float(w << 16); }
; DI float bfhi(unsigned w) { return __uint_as_float(w & 0xffff0000u); }
; DI unsigned pk2(float lo, float hi) { unsigned r; asm("v_cvt_pk_bf16_f32 %0, %1, %2" : "=v"(r) : "v"(lo), "v"(hi)); return r; }
; #define LAS __attribute__((address_space(3)))
; __global__ void __launch_bounds__(256) k_ret_norm(const float* __restrict__ Oraw, const float* __restrict__ gain, const bf16_t* __restrict__ RG, bf16_t* __restrict__ MIXIN) {
;     const int lane = threadIdx.x & 63, w = blockIdx.x * 4 + (threadIdx.x >> 6);
;     const int bh = w >> 12, s = w & 4095, b = bh >> 3, h = bh & 7;
;     const f32x2 v = *(const f32x2*)(Oraw + ((size_t)bh * S + s) * 128 + 2 * lane);
;     const float mu = wave_sum(v.x + v.y) * (1.f / 128.f);
;     const float d0 = v.x - mu, d1 = v.y - mu;
;     const float var = wave_sum(d0 * d0 + d1 * d1) * (1.f / 128.f);
;     const float rs = rsqrtf(var + NORM_EPS);
;     const size_t tok = (size_t)b * S + s;
;     const unsigned g = *(const unsigned*)(RG + tok * 1024 + h * 128 + 2 * lane);
;     *(unsigned*)(MIXIN + tok * D + 1024 + h * 128 + 2 * lane) = pk2(d0 * rs * gain[h * 128 + 2 * lane] * bflo(g), d1 * rs * gain[h * 128 + 2 * lane + 1] * bfhi(g));
; }
; __global__ void __launch_bounds__(NTHR, 2) mega(Args a) {
;     extern __shared__ __attribute__((aligned(16))) unsigned char lds[];
;     Frame F;
;     F.lds = lds; F.ldsl = (LAS unsigned char*)lds; F.ws = a.ws; F.in = a.in; F.out = a.out;
;     F.wg = blockIdx.x; F.nwg = gridDim.x;
;     F.wave = __builtin_amdgcn_readfirstlane(threadIdx.x >> 6);
  - .agpr_count:     0
    .args:
      - .actual_access:  read_only
        .address_space:  global
        .offset:         0
        .size:           8
        .value_kind:     global_buffer
      - .actual_access:  read_only
        .address_space:  global
        .offset:         8
        .size:           8
        .value_kind:     global_buffer
      - .actual_access:  read_only
        .address_space:  global
        .offset:         16
        .size:           8
        .value_kind:     global_buffer
      - .actual_access:  write_only
        .address_space:  global
        .offset:         24
        .size:           8
        .value_kind:     global_buffer
    .group_segment_fixed_size: 0
    .kernarg_segment_align: 8
    .kernarg_segment_size: 32
    .language:       OpenCL C
    .language_version:
      - 2
      - 0
    .max_flat_workgroup_size: 256
    .name:           _Z10k_ret_normPKfS0_PKtPt
    .private_segment_fixed_size: 0
    .sgpr_count:     20
    .sgpr_spill_count: 0
    .symbol:         _Z10k_ret_normPKfS0_PKtPt.kd
    .uniform_work_group_size: 1
    .uses_dynamic_stack: false
    .vgpr_count:     12
    .vgpr_spill_count: 0
    .wavefront_size: 64
  - .agpr_count:     0
    .args:
      - .offset:         0
        .size:           200
        .value_kind:     by_value
      - .offset:         200
        .size:           4
        .value_kind:     hidden_block_count_x
      - .offset:         204
        .size:           4
        .value_kind:     hidden_block_count_y
      - .offset:         208
        .size:           4
        .value_kind:     hidden_block_count_z
      - .offset:         212
        .size:           2
        .value_kind:     hidden_group_size_x
      - .offset:         214
        .size:           2
        .value_kind:     hidden_group_size_y
      - .offset:         216
        .size:           2
        .value_kind:     hidden_group_size_z
      - .offset:         218
        .size:           2
        .value_kind:     hidden_remainder_x
      - .offset:         220
        .size:           2
        .value_kind:     hidden_remainder_y
      - .offset:         222
        .size:           2
        .value_kind:     hidden_remainder_z
      - .offset:         240
        .size:           8
        .value_kind:     hidden_global_offset_x
      - .offset:         248
        .size:           8
        .value_kind:     hidden_global_offset_y
      - .offset:         256
        .size:           8
        .value_kind:     hidden_global_offset_z
      - .offset:         264
        .size:           2
        .value_kind:     hidden_grid_dims
      - .offset:         320
        .size:           4
        .value_kind:     hidden_dynamic_lds_size
    .group_segment_fixed_size: 0
    .kernarg_segment_align: 8
    .kernarg_segment_size: 456
    .language:       OpenCL C
    .language_version:
      - 2
      - 0
    .max_flat_workgroup_size: 512
    .name:           _Z4mega4Args
    .private_segment_fixed_size: 0
    .sgpr_count:     102
    .sgpr_spill_count: 0
    .symbol:         _Z4mega4Args.kd
    .uniform_work_group_size: 1
    .uses_dynamic_stack: false
    .vgpr_count:     256
    .vgpr_spill_count: 0
    .wavefront_size: 64
